# GEMM sub-phases: redundant post-barrier lgkmcnt wait removed; address op fills the m0 wait state instead of s_nop
# baseline (speedup 1.0000x reference)
.LBB0_337:
	s_add_i32 s42, s19, s18
	s_mov_b32 m0, s42
	v_readfirstlane_b32 s6, v192
	v_readfirstlane_b32 s7, v193
	ds_read_b128 v[204:207], v203 offset:16384
	ds_read_b128 v[208:211], v203 offset:17408
	ds_read_b128 v[222:225], v203 offset:18432
	ds_read_b128 v[226:229], v203 offset:19456
	ds_read_b128 v[244:247], v203 offset:20480
	ds_read_b128 v[248:251], v203 offset:21504
	ds_read_b128 v[180:183], v203 offset:22528
	ds_read_b128 v[184:187], v203 offset:23552
	global_load_lds_dwordx4 v166, s[6:7]
	s_add_i32 m0, s42, 0x2000
	s_add_i32 s42, s20, s18
	global_load_lds_dwordx4 v170, s[6:7]
	s_mov_b32 m0, s42
	v_readfirstlane_b32 s6, v196
	v_readfirstlane_b32 s7, v197
	v_lshl_add_u64 v[198:199], v[200:201], 0, v[218:219]
	v_lshl_add_u64 v[200:201], v[200:201], 0, v[168:169]
	v_mov_b32_e32 v167, v219
	v_mov_b32_e32 v171, v219
	v_lshl_add_u64 v[190:191], v[192:193], 0, v[166:167]
	global_load_lds_dwordx4 v166, s[6:7]
	s_add_i32 m0, s42, 0x2000
	v_lshl_add_u64 v[192:193], v[192:193], 0, v[170:171]
	global_load_lds_dwordx4 v170, s[6:7]
	s_mov_b32 m0, s26
	v_lshl_add_u64 v[194:195], v[196:197], 0, v[166:167]
	global_load_lds_dwordx4 v[198:199], off
	s_add_i32 m0, s26, 0x2000
	v_lshl_add_u64 v[196:197], v[196:197], 0, v[170:171]
	global_load_lds_dwordx4 v[200:201], off
	s_waitcnt vmcnt(8)
	s_waitcnt lgkmcnt(0)
	s_barrier
	s_setprio 1
	v_mfma_scale_f32_16x16x128_f8f6f4 v[94:97], v[18:25], v[204:211], v[94:97], v232, v232 op_sel_hi:[0,0,0]
	v_mfma_scale_f32_16x16x128_f8f6f4 v[90:93], v[26:33], v[204:211], v[90:93], v232, v232 op_sel_hi:[0,0,0]
	v_mfma_scale_f32_16x16x128_f8f6f4 v[78:81], v[18:25], v[222:229], v[78:81], v232, v232 op_sel_hi:[0,0,0]
	v_mfma_scale_f32_16x16x128_f8f6f4 v[74:77], v[26:33], v[222:229], v[74:77], v232, v232 op_sel_hi:[0,0,0]
	v_mfma_scale_f32_16x16x128_f8f6f4 v[62:65], v[18:25], v[244:251], v[62:65], v232, v232 op_sel_hi:[0,0,0]
	v_mfma_scale_f32_16x16x128_f8f6f4 v[58:61], v[26:33], v[244:251], v[58:61], v232, v232 op_sel_hi:[0,0,0]
	v_mfma_scale_f32_16x16x128_f8f6f4 v[46:49], v[18:25], v[180:187], v[46:49], v232, v232 op_sel_hi:[0,0,0]
	v_mfma_scale_f32_16x16x128_f8f6f4 v[42:45], v[26:33], v[180:187], v[42:45], v232, v232 op_sel_hi:[0,0,0]
	v_mfma_scale_f32_16x16x128_f8f6f4 v[86:89], v[2:9], v[204:211], v[86:89], v232, v232 op_sel_hi:[0,0,0]
	v_mfma_scale_f32_16x16x128_f8f6f4 v[82:85], v[10:17], v[204:211], v[82:85], v232, v232 op_sel_hi:[0,0,0]
	v_mfma_scale_f32_16x16x128_f8f6f4 v[70:73], v[2:9], v[222:229], v[70:73], v232, v232 op_sel_hi:[0,0,0]
	v_mfma_scale_f32_16x16x128_f8f6f4 v[66:69], v[10:17], v[222:229], v[66:69], v232, v232 op_sel_hi:[0,0,0]
	v_mfma_scale_f32_16x16x128_f8f6f4 v[54:57], v[2:9], v[244:251], v[54:57], v232, v232 op_sel_hi:[0,0,0]
	v_mfma_scale_f32_16x16x128_f8f6f4 v[50:53], v[10:17], v[244:251], v[50:53], v232, v232 op_sel_hi:[0,0,0]
	v_mfma_scale_f32_16x16x128_f8f6f4 v[38:41], v[2:9], v[180:187], v[38:41], v232, v232 op_sel_hi:[0,0,0]
	v_mfma_scale_f32_16x16x128_f8f6f4 v[34:37], v[10:17], v[180:187], v[34:37], v232, v232 op_sel_hi:[0,0,0]
	s_setprio 0
	s_barrier
	v_add_u32_e32 v14, s23, v202
	v_add_u32_e32 v30, s29, v202
	ds_read_b128 v[2:5], v14
	ds_read_b128 v[6:9], v14 offset:1024
	ds_read_b128 v[10:13], v14 offset:2048
	ds_read_b128 v[14:17], v14 offset:3072
	ds_read_b128 v[18:21], v30
	ds_read_b128 v[22:25], v30 offset:1024
	ds_read_b128 v[26:29], v30 offset:2048
	ds_read_b128 v[30:33], v30 offset:3072
	v_lshl_add_u64 v[240:241], v[188:189], 0, v[218:219]
	s_add_i32 m0, s26, 0x4000
	ds_read_b128 v[180:183], v203 offset:32768
	ds_read_b128 v[184:187], v203 offset:33792
	ds_read_b128 v[204:207], v203 offset:34816
	ds_read_b128 v[208:211], v203 offset:35840
	ds_read_b128 v[222:225], v203 offset:36864
	ds_read_b128 v[226:229], v203 offset:37888
	ds_read_b128 v[244:247], v203 offset:38912
	ds_read_b128 v[248:251], v203 offset:39936
	global_load_lds_dwordx4 v[240:241], off
	v_lshl_add_u64 v[188:189], v[188:189], 0, v[168:169]
	s_add_i32 m0, s26, 0x6000
	s_nop 0
	global_load_lds_dwordx4 v[188:189], off
	s_waitcnt vmcnt(8)
	s_waitcnt lgkmcnt(0)
	s_barrier
	s_setprio 1
	v_mfma_scale_f32_16x16x128_f8f6f4 v[158:161], v[2:9], v[180:187], v[158:161], v232, v232 op_sel_hi:[0,0,0]
	v_mfma_scale_f32_16x16x128_f8f6f4 v[154:157], v[10:17], v[180:187], v[154:157], v232, v232 op_sel_hi:[0,0,0]
	v_mfma_scale_f32_16x16x128_f8f6f4 v[142:145], v[2:9], v[204:211], v[142:145], v232, v232 op_sel_hi:[0,0,0]
	v_mfma_scale_f32_16x16x128_f8f6f4 v[138:141], v[10:17], v[204:211], v[138:141], v232, v232 op_sel_hi:[0,0,0]
	v_mfma_scale_f32_16x16x128_f8f6f4 v[126:129], v[2:9], v[222:229], v[126:129], v232, v232 op_sel_hi:[0,0,0]
	v_mfma_scale_f32_16x16x128_f8f6f4 v[122:125], v[10:17], v[222:229], v[122:125], v232, v232 op_sel_hi:[0,0,0]
	v_mfma_scale_f32_16x16x128_f8f6f4 v[110:113], v[2:9], v[244:251], v[110:113], v232, v232 op_sel_hi:[0,0,0]
	v_mfma_scale_f32_16x16x128_f8f6f4 v[106:109], v[10:17], v[244:251], v[106:109], v232, v232 op_sel_hi:[0,0,0]
	v_mfma_scale_f32_16x16x128_f8f6f4 v[150:153], v[18:25], v[180:187], v[150:153], v232, v232 op_sel_hi:[0,0,0]
	v_mfma_scale_f32_16x16x128_f8f6f4 v[146:149], v[26:33], v[180:187], v[146:149], v232, v232 op_sel_hi:[0,0,0]
	v_mfma_scale_f32_16x16x128_f8f6f4 v[134:137], v[18:25], v[204:211], v[134:137], v232, v232 op_sel_hi:[0,0,0]
	v_mfma_scale_f32_16x16x128_f8f6f4 v[130:133], v[26:33], v[204:211], v[130:133], v232, v232 op_sel_hi:[0,0,0]
	v_mfma_scale_f32_16x16x128_f8f6f4 v[118:121], v[18:25], v[222:229], v[118:121], v232, v232 op_sel_hi:[0,0,0]
	v_mfma_scale_f32_16x16x128_f8f6f4 v[114:117], v[26:33], v[222:229], v[114:117], v232, v232 op_sel_hi:[0,0,0]
	v_mfma_scale_f32_16x16x128_f8f6f4 v[102:105], v[18:25], v[244:251], v[102:105], v232, v232 op_sel_hi:[0,0,0]
	v_mfma_scale_f32_16x16x128_f8f6f4 v[98:101], v[26:33], v[244:251], v[98:101], v232, v232 op_sel_hi:[0,0,0]
	s_setprio 0
	s_barrier
	s_mov_b32 m0, s24
	v_lshl_add_u64 v[188:189], v[190:191], 0, s[72:73]
	ds_read_b128 v[180:183], v203 offset:49152
	ds_read_b128 v[184:187], v203 offset:50176
	ds_read_b128 v[204:207], v203 offset:51200
	ds_read_b128 v[208:211], v203 offset:52224
	ds_read_b128 v[222:225], v203 offset:53248
	ds_read_b128 v[226:229], v203 offset:54272
	ds_read_b128 v[244:247], v203 offset:55296
	ds_read_b128 v[248:251], v203 offset:56320
	global_load_lds_dwordx4 v[188:189], off
	s_mov_b32 m0, s25
	v_lshl_add_u64 v[188:189], v[192:193], 0, s[72:73]
	global_load_lds_dwordx4 v[188:189], off
	s_mov_b32 m0, s30
	v_lshl_add_u64 v[188:189], v[194:195], 0, s[72:73]
	global_load_lds_dwordx4 v[188:189], off
	s_mov_b32 m0, s31
	v_lshl_add_u64 v[188:189], v[196:197], 0, s[72:73]
	global_load_lds_dwordx4 v[188:189], off
	s_mov_b32 m0, s27
	v_lshl_add_u64 v[188:189], v[198:199], 0, s[72:73]
	global_load_lds_dwordx4 v[188:189], off
	s_mov_b32 m0, s28
	v_lshl_add_u64 v[188:189], v[200:201], 0, s[72:73]
	global_load_lds_dwordx4 v[188:189], off
	s_waitcnt vmcnt(8)
	s_waitcnt lgkmcnt(0)
	s_barrier
	s_setprio 1
	v_mfma_scale_f32_16x16x128_f8f6f4 v[94:97], v[2:9], v[180:187], v[94:97], v232, v232 op_sel_hi:[0,0,0]
	v_mfma_scale_f32_16x16x128_f8f6f4 v[90:93], v[10:17], v[180:187], v[90:93], v232, v232 op_sel_hi:[0,0,0]
	v_mfma_scale_f32_16x16x128_f8f6f4 v[78:81], v[2:9], v[204:211], v[78:81], v232, v232 op_sel_hi:[0,0,0]
	v_mfma_scale_f32_16x16x128_f8f6f4 v[74:77], v[10:17], v[204:211], v[74:77], v232, v232 op_sel_hi:[0,0,0]
	v_mfma_scale_f32_16x16x128_f8f6f4 v[62:65], v[2:9], v[222:229], v[62:65], v232, v232 op_sel_hi:[0,0,0]
	v_mfma_scale_f32_16x16x128_f8f6f4 v[58:61], v[10:17], v[222:229], v[58:61], v232, v232 op_sel_hi:[0,0,0]
	v_mfma_scale_f32_16x16x128_f8f6f4 v[46:49], v[2:9], v[244:251], v[46:49], v232, v232 op_sel_hi:[0,0,0]
	v_mfma_scale_f32_16x16x128_f8f6f4 v[42:45], v[10:17], v[244:251], v[42:45], v232, v232 op_sel_hi:[0,0,0]
	v_mfma_scale_f32_16x16x128_f8f6f4 v[86:89], v[18:25], v[180:187], v[86:89], v232, v232 op_sel_hi:[0,0,0]
	v_mfma_scale_f32_16x16x128_f8f6f4 v[82:85], v[26:33], v[180:187], v[82:85], v232, v232 op_sel_hi:[0,0,0]
	v_mfma_scale_f32_16x16x128_f8f6f4 v[70:73], v[18:25], v[204:211], v[70:73], v232, v232 op_sel_hi:[0,0,0]
	v_mfma_scale_f32_16x16x128_f8f6f4 v[66:69], v[26:33], v[204:211], v[66:69], v232, v232 op_sel_hi:[0,0,0]
	v_mfma_scale_f32_16x16x128_f8f6f4 v[54:57], v[18:25], v[222:229], v[54:57], v232, v232 op_sel_hi:[0,0,0]
	v_mfma_scale_f32_16x16x128_f8f6f4 v[50:53], v[26:33], v[222:229], v[50:53], v232, v232 op_sel_hi:[0,0,0]
	v_mfma_scale_f32_16x16x128_f8f6f4 v[38:41], v[18:25], v[244:251], v[38:41], v232, v232 op_sel_hi:[0,0,0]
	v_mfma_scale_f32_16x16x128_f8f6f4 v[34:37], v[26:33], v[244:251], v[34:37], v232, v232 op_sel_hi:[0,0,0]
	s_setprio 0
	s_barrier
	s_add_i32 s41, s41, 2
	s_add_u32 s14, s14, 0x100
	s_addc_u32 s15, s15, 0
	s_cmp_gt_u32 s41, 5
	s_cbranch_scc1 .LBB0_345
.LBB0_338:
	v_add_u32_e32 v2, s19, v202
	v_add_u32_e32 v14, s20, v202
	ds_read_b128 v[18:21], v2
	ds_read_b128 v[22:25], v2 offset:1024
	ds_read_b128 v[26:29], v2 offset:2048
	ds_read_b128 v[30:33], v2 offset:3072
	ds_read_b128 v[2:5], v14
	ds_read_b128 v[6:9], v14 offset:1024
	ds_read_b128 v[10:13], v14 offset:2048
	ds_read_b128 v[14:17], v14 offset:3072
	v_lshl_add_u64 v[188:189], v[176:177], 0, s[14:15]
	v_lshl_add_u64 v[180:181], v[188:189], 0, v[218:219]
	v_lshl_add_u64 v[180:181], v[180:181], 0, s[74:75]
	s_add_i32 m0, s26, 0xc000
	v_mov_b32_e32 v169, v219
	ds_read_b128 v[190:193], v203
	ds_read_b128 v[194:197], v203 offset:1024
	ds_read_b128 v[204:207], v203 offset:2048
	ds_read_b128 v[208:211], v203 offset:3072
	ds_read_b128 v[244:247], v203 offset:4096
	ds_read_b128 v[248:251], v203 offset:5120
	ds_read_b128 v[222:225], v203 offset:6144
	ds_read_b128 v[226:229], v203 offset:7168
	global_load_lds_dwordx4 v[180:181], off
	v_lshl_add_u64 v[180:181], v[188:189], 0, v[168:169]
	v_lshl_add_u64 v[180:181], v[180:181], 0, s[74:75]
	s_add_i32 m0, s26, 0xe000
	s_nop 0
	global_load_lds_dwordx4 v[180:181], off
	s_waitcnt vmcnt(8)
	s_waitcnt lgkmcnt(0)
	s_barrier
	s_setprio 1
	v_mfma_scale_f32_16x16x128_f8f6f4 v[158:161], v[18:25], v[190:197], v[158:161], v232, v232 op_sel_hi:[0,0,0]
	v_mfma_scale_f32_16x16x128_f8f6f4 v[154:157], v[26:33], v[190:197], v[154:157], v232, v232 op_sel_hi:[0,0,0]
	v_mfma_scale_f32_16x16x128_f8f6f4 v[142:145], v[18:25], v[204:211], v[142:145], v232, v232 op_sel_hi:[0,0,0]
	v_mfma_scale_f32_16x16x128_f8f6f4 v[138:141], v[26:33], v[204:211], v[138:141], v232, v232 op_sel_hi:[0,0,0]
	v_mfma_scale_f32_16x16x128_f8f6f4 v[126:129], v[18:25], v[244:251], v[126:129], v232, v232 op_sel_hi:[0,0,0]
	v_mfma_scale_f32_16x16x128_f8f6f4 v[122:125], v[26:33], v[244:251], v[122:125], v232, v232 op_sel_hi:[0,0,0]
	v_mfma_scale_f32_16x16x128_f8f6f4 v[110:113], v[18:25], v[222:229], v[110:113], v232, v232 op_sel_hi:[0,0,0]
	v_mfma_scale_f32_16x16x128_f8f6f4 v[106:109], v[26:33], v[222:229], v[106:109], v232, v232 op_sel_hi:[0,0,0]
	v_mfma_scale_f32_16x16x128_f8f6f4 v[150:153], v[2:9], v[190:197], v[150:153], v232, v232 op_sel_hi:[0,0,0]
	v_mfma_scale_f32_16x16x128_f8f6f4 v[146:149], v[10:17], v[190:197], v[146:149], v232, v232 op_sel_hi:[0,0,0]
	v_mfma_scale_f32_16x16x128_f8f6f4 v[134:137], v[2:9], v[204:211], v[134:137], v232, v232 op_sel_hi:[0,0,0]
	v_mfma_scale_f32_16x16x128_f8f6f4 v[130:133], v[10:17], v[204:211], v[130:133], v232, v232 op_sel_hi:[0,0,0]
	v_mfma_scale_f32_16x16x128_f8f6f4 v[118:121], v[2:9], v[244:251], v[118:121], v232, v232 op_sel_hi:[0,0,0]
	v_mfma_scale_f32_16x16x128_f8f6f4 v[114:117], v[10:17], v[244:251], v[114:117], v232, v232 op_sel_hi:[0,0,0]
	v_mfma_scale_f32_16x16x128_f8f6f4 v[102:105], v[2:9], v[222:229], v[102:105], v232, v232 op_sel_hi:[0,0,0]
	v_mfma_scale_f32_16x16x128_f8f6f4 v[98:101], v[10:17], v[222:229], v[98:101], v232, v232 op_sel_hi:[0,0,0]
	s_cmpk_lg_i32 s14, 0x300
	s_setprio 0
	s_barrier
	s_cbranch_scc0 .LBB0_340
	s_mov_b64 s[6:7], 0x20100
	v_lshl_add_u64 v[200:201], v[188:189], 0, s[76:77]
	v_lshl_add_u64 v[180:181], v[178:179], 0, s[14:15]
	v_lshl_add_u64 v[188:189], v[188:189], 0, s[6:7]
	s_mov_b64 s[6:7], 0x8100
	v_lshl_add_u64 v[192:193], v[180:181], 0, s[76:77]
	v_lshl_add_u64 v[196:197], v[180:181], 0, s[6:7]
	s_cbranch_execnz .LBB0_337
	s_branch .LBB0_341

.LBB0_551:
	s_mov_b64 s[6:7], 0x2000
	s_add_i32 s33, s15, s14
	v_lshl_add_u64 v[66:67], v[162:163], 0, s[6:7]
	s_mov_b32 m0, s33
	v_readfirstlane_b32 s6, v162
	v_readfirstlane_b32 s7, v163
	ds_read_b128 v[122:125], v175 offset:16384
	ds_read_b128 v[126:129], v175 offset:17408
	ds_read_b128 v[176:179], v175 offset:18432
	ds_read_b128 v[180:183], v175 offset:19456
	ds_read_b128 v[184:187], v175 offset:20480
	ds_read_b128 v[188:191], v175 offset:21504
	ds_read_b128 v[192:195], v175 offset:22528
	ds_read_b128 v[196:199], v175 offset:23552
	global_load_lds_dwordx4 v152, s[6:7]
	s_add_i32 m0, s33, 0x2000
	s_add_i32 s33, s16, s14
	global_load_lds_dwordx4 v156, s[6:7]
	s_mov_b32 m0, s33
	v_readfirstlane_b32 s6, v66
	v_readfirstlane_b32 s7, v67
	v_lshl_add_u64 v[170:171], v[164:165], 0, v[218:219]
	v_lshl_add_u64 v[172:173], v[164:165], 0, v[154:155]
	v_mov_b32_e32 v153, v219
	v_mov_b32_e32 v157, v219
	v_lshl_add_u64 v[166:167], v[162:163], 0, v[152:153]
	global_load_lds_dwordx4 v152, s[6:7]
	s_add_i32 m0, s33, 0x2000
	v_lshl_add_u64 v[168:169], v[162:163], 0, v[156:157]
	global_load_lds_dwordx4 v156, s[6:7]
	s_mov_b32 m0, s20
	s_nop 0
	global_load_lds_dwordx4 v[170:171], off
	s_add_i32 m0, s20, 0x2000
	s_nop 0
	global_load_lds_dwordx4 v[172:173], off
	s_waitcnt vmcnt(8)
	s_waitcnt lgkmcnt(0)
	s_barrier
	s_setprio 1
	v_mov_b64_e32 v[136:137], s[90:91]
	v_mov_b64_e32 v[132:133], s[90:91]
	v_mov_b64_e32 v[120:121], s[90:91]
	v_mov_b64_e32 v[116:117], s[90:91]
	v_mov_b64_e32 v[96:97], s[90:91]
	v_mov_b64_e32 v[92:93], s[90:91]
	v_mov_b64_e32 v[70:71], s[88:89]
	v_mov_b64_e32 v[134:135], s[88:89]
	v_mov_b64_e32 v[130:131], s[88:89]
	v_mov_b64_e32 v[118:119], s[88:89]
	v_mov_b64_e32 v[114:115], s[88:89]
	v_mov_b64_e32 v[94:95], s[88:89]
	v_mov_b64_e32 v[90:91], s[88:89]
	v_mov_b64_e32 v[72:73], s[90:91]
	v_mov_b64_e32 v[66:67], s[88:89]
	s_waitcnt lgkmcnt(0)
	v_mfma_scale_f32_16x16x128_f8f6f4 v[134:137], v[10:17], v[122:129], v[134:137], v232, v232 op_sel_hi:[0,0,0]
	v_mfma_scale_f32_16x16x128_f8f6f4 v[130:133], v[26:33], v[122:129], v[130:133], v232, v232 op_sel_hi:[0,0,0]
	v_mfma_scale_f32_16x16x128_f8f6f4 v[118:121], v[10:17], v[176:183], v[118:121], v232, v232 op_sel_hi:[0,0,0]
	v_mfma_scale_f32_16x16x128_f8f6f4 v[114:117], v[26:33], v[176:183], v[114:117], v232, v232 op_sel_hi:[0,0,0]
	v_mfma_scale_f32_16x16x128_f8f6f4 v[94:97], v[10:17], v[184:191], v[94:97], v232, v232 op_sel_hi:[0,0,0]
	v_mfma_scale_f32_16x16x128_f8f6f4 v[90:93], v[26:33], v[184:191], v[90:93], v232, v232 op_sel_hi:[0,0,0]
	v_mfma_scale_f32_16x16x128_f8f6f4 v[70:73], v[10:17], v[192:199], v[70:73], v232, v232 op_sel_hi:[0,0,0]
	v_mov_b64_e32 v[10:11], s[88:89]
	v_mov_b64_e32 v[68:69], s[90:91]
	v_mov_b64_e32 v[12:13], s[90:91]
	v_mfma_scale_f32_16x16x128_f8f6f4 v[10:13], v[26:33], v[192:199], v[10:13], v232, v232 op_sel_hi:[0,0,0]
	v_mov_b64_e32 v[144:145], s[90:91]
	v_mov_b64_e32 v[140:141], s[90:91]
	v_mov_b64_e32 v[142:143], s[88:89]
	v_mov_b64_e32 v[138:139], s[88:89]
	v_mfma_scale_f32_16x16x128_f8f6f4 v[142:145], v[2:9], v[122:129], v[142:145], v232, v232 op_sel_hi:[0,0,0]
	v_mfma_scale_f32_16x16x128_f8f6f4 v[138:141], v[18:25], v[122:129], v[138:141], v232, v232 op_sel_hi:[0,0,0]
	v_mov_b64_e32 v[128:129], s[90:91]
	v_mov_b64_e32 v[124:125], s[90:91]
	v_mov_b64_e32 v[30:31], s[88:89]
	v_mov_b64_e32 v[26:27], s[88:89]
	v_mov_b64_e32 v[14:15], s[88:89]
	v_mov_b64_e32 v[126:127], s[88:89]
	v_mov_b64_e32 v[122:123], s[88:89]
	v_mov_b64_e32 v[32:33], s[90:91]
	v_mov_b64_e32 v[28:29], s[90:91]
	v_mov_b64_e32 v[16:17], s[90:91]
	v_mfma_scale_f32_16x16x128_f8f6f4 v[126:129], v[2:9], v[176:183], v[126:129], v232, v232 op_sel_hi:[0,0,0]
	v_mfma_scale_f32_16x16x128_f8f6f4 v[122:125], v[18:25], v[176:183], v[122:125], v232, v232 op_sel_hi:[0,0,0]
	v_mfma_scale_f32_16x16x128_f8f6f4 v[30:33], v[2:9], v[184:191], v[30:33], v232, v232 op_sel_hi:[0,0,0]
	v_mfma_scale_f32_16x16x128_f8f6f4 v[26:29], v[18:25], v[184:191], v[26:29], v232, v232 op_sel_hi:[0,0,0]
	v_mfma_scale_f32_16x16x128_f8f6f4 v[14:17], v[2:9], v[192:199], v[14:17], v232, v232 op_sel_hi:[0,0,0]
	v_mfma_scale_f32_16x16x128_f8f6f4 v[66:69], v[18:25], v[192:199], v[66:69], v232, v232 op_sel_hi:[0,0,0]
	s_setprio 0
	s_barrier
	v_add_u32_e32 v22, s17, v174
	v_add_u32_e32 v153, s23, v174
	ds_read_b128 v[2:5], v22
	ds_read_b128 v[6:9], v22 offset:1024
	ds_read_b128 v[18:21], v22 offset:2048
	ds_read_b128 v[22:25], v22 offset:3072
	ds_read_b128 v[176:179], v153
	ds_read_b128 v[180:183], v153 offset:1024
	ds_read_b128 v[184:187], v153 offset:2048
	ds_read_b128 v[188:191], v153 offset:3072
	v_lshl_add_u64 v[164:165], v[164:165], 0, s[60:61]
	v_lshl_add_u64 v[216:217], v[164:165], 0, v[218:219]
	s_add_i32 m0, s20, 0x4000
	ds_read_b128 v[192:195], v175 offset:32768
	ds_read_b128 v[196:199], v175 offset:33792
	ds_read_b128 v[200:203], v175 offset:34816
	ds_read_b128 v[204:207], v175 offset:35840
	ds_read_b128 v[208:211], v175 offset:36864
	ds_read_b128 v[212:215], v175 offset:37888
	ds_read_b128 v[222:225], v175 offset:38912
	ds_read_b128 v[226:229], v175 offset:39936
	global_load_lds_dwordx4 v[216:217], off
	v_lshl_add_u64 v[164:165], v[164:165], 0, v[154:155]
	s_add_i32 m0, s20, 0x6000
	s_nop 0
	global_load_lds_dwordx4 v[164:165], off
	s_waitcnt vmcnt(8)
	s_waitcnt lgkmcnt(0)
	s_barrier
	s_setprio 1
	v_mfma_scale_f32_16x16x128_f8f6f4 v[102:105], v[2:9], v[192:199], v[102:105], v232, v232 op_sel_hi:[0,0,0]
	v_mfma_scale_f32_16x16x128_f8f6f4 v[98:101], v[18:25], v[192:199], v[98:101], v232, v232 op_sel_hi:[0,0,0]
	v_mfma_scale_f32_16x16x128_f8f6f4 v[78:81], v[2:9], v[200:207], v[78:81], v232, v232 op_sel_hi:[0,0,0]
	v_mfma_scale_f32_16x16x128_f8f6f4 v[74:77], v[18:25], v[200:207], v[74:77], v232, v232 op_sel_hi:[0,0,0]
	v_mfma_scale_f32_16x16x128_f8f6f4 v[58:61], v[2:9], v[208:215], v[58:61], v232, v232 op_sel_hi:[0,0,0]
	v_mfma_scale_f32_16x16x128_f8f6f4 v[50:53], v[18:25], v[208:215], v[50:53], v232, v232 op_sel_hi:[0,0,0]
	v_mfma_scale_f32_16x16x128_f8f6f4 v[42:45], v[2:9], v[222:229], v[42:45], v232, v232 op_sel_hi:[0,0,0]
	v_mfma_scale_f32_16x16x128_f8f6f4 v[38:41], v[18:25], v[222:229], v[38:41], v232, v232 op_sel_hi:[0,0,0]
	v_mfma_scale_f32_16x16x128_f8f6f4 v[110:113], v[176:183], v[192:199], v[110:113], v232, v232 op_sel_hi:[0,0,0]
	v_mfma_scale_f32_16x16x128_f8f6f4 v[106:109], v[184:191], v[192:199], v[106:109], v232, v232 op_sel_hi:[0,0,0]
	v_mfma_scale_f32_16x16x128_f8f6f4 v[86:89], v[176:183], v[200:207], v[86:89], v232, v232 op_sel_hi:[0,0,0]
	v_mfma_scale_f32_16x16x128_f8f6f4 v[82:85], v[184:191], v[200:207], v[82:85], v232, v232 op_sel_hi:[0,0,0]
	v_mfma_scale_f32_16x16x128_f8f6f4 v[62:65], v[176:183], v[208:215], v[62:65], v232, v232 op_sel_hi:[0,0,0]
	v_mfma_scale_f32_16x16x128_f8f6f4 v[54:57], v[184:191], v[208:215], v[54:57], v232, v232 op_sel_hi:[0,0,0]
	v_mfma_scale_f32_16x16x128_f8f6f4 v[46:49], v[176:183], v[222:229], v[46:49], v232, v232 op_sel_hi:[0,0,0]
	v_mfma_scale_f32_16x16x128_f8f6f4 v[34:37], v[184:191], v[222:229], v[34:37], v232, v232 op_sel_hi:[0,0,0]
	s_setprio 0
	s_barrier
	s_mov_b32 m0, s18
	v_lshl_add_u64 v[164:165], v[166:167], 0, s[72:73]
	s_mov_b64 s[6:7], 0x2080
	ds_read_b128 v[192:195], v175 offset:49152
	ds_read_b128 v[196:199], v175 offset:50176
	ds_read_b128 v[200:203], v175 offset:51200
	ds_read_b128 v[204:207], v175 offset:52224
	ds_read_b128 v[208:211], v175 offset:53248
	ds_read_b128 v[212:215], v175 offset:54272
	ds_read_b128 v[222:225], v175 offset:55296
	ds_read_b128 v[226:229], v175 offset:56320
	global_load_lds_dwordx4 v[164:165], off
	v_lshl_add_u64 v[164:165], v[168:169], 0, s[72:73]
	s_mov_b32 m0, s19
	v_lshl_add_u64 v[162:163], v[162:163], 0, s[6:7]
	global_load_lds_dwordx4 v[164:165], off
	v_readfirstlane_b32 s6, v162
	v_readfirstlane_b32 s7, v163
	s_mov_b32 m0, s24
	v_lshl_add_u64 v[162:163], v[170:171], 0, s[72:73]
	s_nop 2
	global_load_lds_dwordx4 v152, s[6:7]
	s_mov_b32 m0, s25
	s_nop 0
	global_load_lds_dwordx4 v156, s[6:7]
	s_mov_b32 m0, s21
	s_nop 0
	global_load_lds_dwordx4 v[162:163], off
	s_mov_b32 m0, s22
	v_lshl_add_u64 v[162:163], v[172:173], 0, s[72:73]
	global_load_lds_dwordx4 v[162:163], off
	s_waitcnt vmcnt(8)
	s_waitcnt lgkmcnt(0)
	s_barrier
	s_setprio 1
	v_mfma_scale_f32_16x16x128_f8f6f4 v[134:137], v[2:9], v[192:199], v[134:137], v232, v232 op_sel_hi:[0,0,0]
	v_mfma_scale_f32_16x16x128_f8f6f4 v[130:133], v[18:25], v[192:199], v[130:133], v232, v232 op_sel_hi:[0,0,0]
	v_mfma_scale_f32_16x16x128_f8f6f4 v[118:121], v[2:9], v[200:207], v[118:121], v232, v232 op_sel_hi:[0,0,0]
	v_mfma_scale_f32_16x16x128_f8f6f4 v[114:117], v[18:25], v[200:207], v[114:117], v232, v232 op_sel_hi:[0,0,0]
	v_mfma_scale_f32_16x16x128_f8f6f4 v[94:97], v[2:9], v[208:215], v[94:97], v232, v232 op_sel_hi:[0,0,0]
	v_mfma_scale_f32_16x16x128_f8f6f4 v[90:93], v[18:25], v[208:215], v[90:93], v232, v232 op_sel_hi:[0,0,0]
	v_mfma_scale_f32_16x16x128_f8f6f4 v[70:73], v[2:9], v[222:229], v[70:73], v232, v232 op_sel_hi:[0,0,0]
	v_mfma_scale_f32_16x16x128_f8f6f4 v[10:13], v[18:25], v[222:229], v[10:13], v232, v232 op_sel_hi:[0,0,0]
	v_mfma_scale_f32_16x16x128_f8f6f4 v[142:145], v[176:183], v[192:199], v[142:145], v232, v232 op_sel_hi:[0,0,0]
	v_mfma_scale_f32_16x16x128_f8f6f4 v[138:141], v[184:191], v[192:199], v[138:141], v232, v232 op_sel_hi:[0,0,0]
	v_mfma_scale_f32_16x16x128_f8f6f4 v[126:129], v[176:183], v[200:207], v[126:129], v232, v232 op_sel_hi:[0,0,0]
	v_mfma_scale_f32_16x16x128_f8f6f4 v[122:125], v[184:191], v[200:207], v[122:125], v232, v232 op_sel_hi:[0,0,0]
	v_mfma_scale_f32_16x16x128_f8f6f4 v[30:33], v[176:183], v[208:215], v[30:33], v232, v232 op_sel_hi:[0,0,0]
	v_mfma_scale_f32_16x16x128_f8f6f4 v[26:29], v[184:191], v[208:215], v[26:29], v232, v232 op_sel_hi:[0,0,0]
	v_mfma_scale_f32_16x16x128_f8f6f4 v[14:17], v[176:183], v[222:229], v[14:17], v232, v232 op_sel_hi:[0,0,0]
	v_mfma_scale_f32_16x16x128_f8f6f4 v[66:69], v[184:191], v[222:229], v[66:69], v232, v232 op_sel_hi:[0,0,0]
	s_setprio 0
	s_barrier
	s_andn2_b64 vcc, exec, s[10:11]
	s_cbranch_vccnz .LBB0_553
	s_barrier

.LBB0_876:
	v_add_u32_e32 v196, s39, v182
	ds_read_b128 v[2:5], v196
	ds_read_b128 v[6:9], v196 offset:1024
	ds_read_b128 v[10:13], v196 offset:2048
	ds_read_b128 v[14:17], v196 offset:3072
	s_mul_hi_u32 s4, s61, 0xaaaaaaab
	s_lshr_b32 s19, s4, 2
	s_add_u32 s6, s24, 0x10080
	s_addc_u32 s7, s25, 0
	s_add_i32 s4, s44, 0xc000
	s_mov_b32 m0, s4
	s_add_i32 s5, s44, 0xe000
	ds_read_b128 v[22:25], v183
	ds_read_b128 v[26:29], v183 offset:1024
	ds_read_b128 v[30:33], v183 offset:2048
	ds_read_b128 v[34:37], v183 offset:3072
	ds_read_b128 v[38:41], v183 offset:4096
	ds_read_b128 v[42:45], v183 offset:5120
	ds_read_b128 v[82:85], v183 offset:6144
	ds_read_b128 v[86:89], v183 offset:7168
	global_load_lds_dwordx4 v218, s[6:7]
	s_mov_b32 m0, s5
	v_mov_b32_e32 v97, v219
	global_load_lds_dwordx4 v96, s[6:7]
	s_waitcnt vmcnt(6)
	s_waitcnt lgkmcnt(0)
	s_barrier
	s_setprio 1
	v_mov_b64_e32 v[18:19], s[88:89]
	v_mov_b64_e32 v[78:79], s[88:89]
	v_mov_b64_e32 v[74:75], s[88:89]
	v_mov_b64_e32 v[70:71], s[88:89]
	v_mov_b64_e32 v[66:67], s[88:89]
	v_mov_b64_e32 v[62:63], s[88:89]
	v_mov_b64_e32 v[58:59], s[88:89]
	v_mov_b64_e32 v[54:55], s[88:89]
	v_mov_b64_e32 v[50:51], s[88:89]
	v_mov_b64_e32 v[20:21], s[90:91]
	v_mov_b64_e32 v[80:81], s[90:91]
	v_mov_b64_e32 v[76:77], s[90:91]
	v_mov_b64_e32 v[72:73], s[90:91]
	v_mov_b64_e32 v[68:69], s[90:91]
	v_mov_b64_e32 v[64:65], s[90:91]
	v_mov_b64_e32 v[60:61], s[90:91]
	v_mov_b64_e32 v[56:57], s[90:91]
	v_mov_b64_e32 v[52:53], s[90:91]
	s_waitcnt lgkmcnt(0)
	v_mfma_scale_f32_16x16x128_f8f6f4 v[78:81], v[2:9], v[22:29], v[78:81], v232, v232 op_sel_hi:[0,0,0]
	v_mfma_scale_f32_16x16x128_f8f6f4 v[74:77], v[10:17], v[22:29], v[74:77], v232, v232 op_sel_hi:[0,0,0]
	v_mfma_scale_f32_16x16x128_f8f6f4 v[70:73], v[2:9], v[30:37], v[70:73], v232, v232 op_sel_hi:[0,0,0]
	v_mfma_scale_f32_16x16x128_f8f6f4 v[66:69], v[10:17], v[30:37], v[66:69], v232, v232 op_sel_hi:[0,0,0]
	v_mfma_scale_f32_16x16x128_f8f6f4 v[62:65], v[2:9], v[38:45], v[62:65], v232, v232 op_sel_hi:[0,0,0]
	v_mfma_scale_f32_16x16x128_f8f6f4 v[58:61], v[10:17], v[38:45], v[58:61], v232, v232 op_sel_hi:[0,0,0]
	v_mfma_scale_f32_16x16x128_f8f6f4 v[54:57], v[2:9], v[82:89], v[54:57], v232, v232 op_sel_hi:[0,0,0]
	v_mfma_scale_f32_16x16x128_f8f6f4 v[50:53], v[10:17], v[82:89], v[50:53], v232, v232 op_sel_hi:[0,0,0]
	s_setprio 0
	s_barrier
	v_mov_b32_e32 v95, v219
	v_lshl_add_u64 v[92:93], s[26:27], 0, v[94:95]
	v_mov_b32_e32 v99, v219
	s_mov_b32 m0, s40
	v_lshl_add_u64 v[30:31], v[92:93], 0, s[76:77]
	v_lshl_add_u64 v[180:181], s[26:27], 0, v[98:99]
	ds_read_b128 v[22:25], v183 offset:16384
	ds_read_b128 v[26:29], v183 offset:17408
	ds_read_b128 v[82:85], v183 offset:18432
	ds_read_b128 v[86:89], v183 offset:19456
	ds_read_b128 v[164:167], v183 offset:20480
	ds_read_b128 v[168:171], v183 offset:21504
	ds_read_b128 v[172:175], v183 offset:22528
	ds_read_b128 v[176:179], v183 offset:23552
	global_load_lds_dwordx4 v[30:31], off
	v_lshl_add_u64 v[32:33], v[180:181], 0, s[76:77]
	s_mov_b32 m0, s41
	v_lshl_add_u64 v[192:193], s[24:25], 0, v[218:219]
	global_load_lds_dwordx4 v[32:33], off
	v_lshl_add_u64 v[194:195], s[24:25], 0, v[96:97]
	v_lshl_add_u64 v[30:31], v[192:193], 0, s[76:77]
	s_mov_b32 m0, s44
	s_add_u32 s6, s24, 0x10100
	global_load_lds_dwordx4 v[30:31], off
	v_lshl_add_u64 v[30:31], v[194:195], 0, s[76:77]
	s_mov_b32 m0, s45
	s_addc_u32 s7, s25, 0
	global_load_lds_dwordx4 v[30:31], off
	s_waitcnt vmcnt(6)
	s_waitcnt lgkmcnt(0)
	s_barrier
	s_setprio 1
	v_mov_b64_e32 v[46:47], s[88:89]
	v_mov_b64_e32 v[42:43], s[88:89]
	v_mov_b64_e32 v[48:49], s[90:91]
	v_mov_b64_e32 v[44:45], s[90:91]
	s_waitcnt lgkmcnt(0)
	v_mfma_scale_f32_16x16x128_f8f6f4 v[46:49], v[2:9], v[22:29], v[46:49], v232, v232 op_sel_hi:[0,0,0]
	v_mfma_scale_f32_16x16x128_f8f6f4 v[42:45], v[10:17], v[22:29], v[42:45], v232, v232 op_sel_hi:[0,0,0]
	v_mov_b64_e32 v[38:39], s[88:89]
	v_mov_b64_e32 v[34:35], s[88:89]
	v_mov_b64_e32 v[30:31], s[88:89]
	v_mov_b64_e32 v[26:27], s[88:89]
	v_mov_b64_e32 v[22:23], s[88:89]
	v_mov_b64_e32 v[40:41], s[90:91]
	v_mov_b64_e32 v[36:37], s[90:91]
	v_mov_b64_e32 v[32:33], s[90:91]
	v_mov_b64_e32 v[28:29], s[90:91]
	v_mov_b64_e32 v[24:25], s[90:91]
	v_mfma_scale_f32_16x16x128_f8f6f4 v[38:41], v[2:9], v[82:89], v[38:41], v232, v232 op_sel_hi:[0,0,0]
	v_mfma_scale_f32_16x16x128_f8f6f4 v[34:37], v[10:17], v[82:89], v[34:37], v232, v232 op_sel_hi:[0,0,0]
	v_mfma_scale_f32_16x16x128_f8f6f4 v[30:33], v[2:9], v[164:171], v[30:33], v232, v232 op_sel_hi:[0,0,0]
	v_mfma_scale_f32_16x16x128_f8f6f4 v[26:29], v[10:17], v[164:171], v[26:29], v232, v232 op_sel_hi:[0,0,0]
	v_mfma_scale_f32_16x16x128_f8f6f4 v[22:25], v[2:9], v[172:179], v[22:25], v232, v232 op_sel_hi:[0,0,0]
	v_mfma_scale_f32_16x16x128_f8f6f4 v[18:21], v[10:17], v[172:179], v[18:21], v232, v232 op_sel_hi:[0,0,0]
	s_setprio 0
	s_barrier
	v_add_u32_e32 v82, s48, v182
	ds_read_b128 v[2:5], v82
	ds_read_b128 v[6:9], v82 offset:1024
	ds_read_b128 v[10:13], v82 offset:2048
	ds_read_b128 v[14:17], v82 offset:3072
	s_mov_b32 m0, s46
	ds_read_b128 v[84:87], v183 offset:32768
	ds_read_b128 v[88:91], v183 offset:33792
	ds_read_b128 v[164:167], v183 offset:34816
	ds_read_b128 v[168:171], v183 offset:35840
	ds_read_b128 v[172:175], v183 offset:36864
	ds_read_b128 v[176:179], v183 offset:37888
	ds_read_b128 v[184:187], v183 offset:38912
	ds_read_b128 v[188:191], v183 offset:39936
	global_load_lds_dwordx4 v218, s[6:7]
	s_mov_b32 m0, s47
	s_nop 0
	global_load_lds_dwordx4 v96, s[6:7]
	s_waitcnt vmcnt(6)
	s_waitcnt lgkmcnt(0)
	s_barrier
	s_setprio 1
	v_mfma_scale_f32_16x16x128_f8f6f4 v[78:81], v[2:9], v[84:91], v[78:81], v232, v232 op_sel_hi:[0,0,0]
	v_mfma_scale_f32_16x16x128_f8f6f4 v[74:77], v[10:17], v[84:91], v[74:77], v232, v232 op_sel_hi:[0,0,0]
	v_mfma_scale_f32_16x16x128_f8f6f4 v[70:73], v[2:9], v[164:171], v[70:73], v232, v232 op_sel_hi:[0,0,0]
	v_mfma_scale_f32_16x16x128_f8f6f4 v[66:69], v[10:17], v[164:171], v[66:69], v232, v232 op_sel_hi:[0,0,0]
	v_mfma_scale_f32_16x16x128_f8f6f4 v[62:65], v[2:9], v[172:179], v[62:65], v232, v232 op_sel_hi:[0,0,0]
	v_mfma_scale_f32_16x16x128_f8f6f4 v[58:61], v[10:17], v[172:179], v[58:61], v232, v232 op_sel_hi:[0,0,0]
	v_mfma_scale_f32_16x16x128_f8f6f4 v[54:57], v[2:9], v[184:191], v[54:57], v232, v232 op_sel_hi:[0,0,0]
	v_mfma_scale_f32_16x16x128_f8f6f4 v[50:53], v[10:17], v[184:191], v[50:53], v232, v232 op_sel_hi:[0,0,0]
	s_setprio 0
	s_barrier
	s_mov_b64 s[6:7], 0x180
	s_mov_b32 m0, s49
	v_lshl_add_u64 v[92:93], v[92:93], 0, s[6:7]
	ds_read_b128 v[84:87], v183 offset:49152
	ds_read_b128 v[88:91], v183 offset:50176
	ds_read_b128 v[164:167], v183 offset:51200
	ds_read_b128 v[168:171], v183 offset:52224
	ds_read_b128 v[172:175], v183 offset:53248
	ds_read_b128 v[176:179], v183 offset:54272
	ds_read_b128 v[184:187], v183 offset:55296
	ds_read_b128 v[188:191], v183 offset:56320
	global_load_lds_dwordx4 v[92:93], off
	s_mov_b32 m0, s50
	v_lshl_add_u64 v[180:181], v[180:181], 0, s[6:7]
	global_load_lds_dwordx4 v[180:181], off
	s_nop 0
	s_mov_b32 m0, s51
	v_lshl_add_u64 v[92:93], v[192:193], 0, s[6:7]
	global_load_lds_dwordx4 v[92:93], off
	s_mov_b32 m0, s56
	v_lshl_add_u64 v[92:93], v[194:195], 0, s[6:7]
	global_load_lds_dwordx4 v[92:93], off
	s_waitcnt vmcnt(6)
	s_waitcnt lgkmcnt(0)
	s_barrier
	s_setprio 1
	v_mfma_scale_f32_16x16x128_f8f6f4 v[46:49], v[2:9], v[84:91], v[46:49], v232, v232 op_sel_hi:[0,0,0]
	v_mfma_scale_f32_16x16x128_f8f6f4 v[42:45], v[10:17], v[84:91], v[42:45], v232, v232 op_sel_hi:[0,0,0]
	v_mfma_scale_f32_16x16x128_f8f6f4 v[38:41], v[2:9], v[164:171], v[38:41], v232, v232 op_sel_hi:[0,0,0]
	v_mfma_scale_f32_16x16x128_f8f6f4 v[34:37], v[10:17], v[164:171], v[34:37], v232, v232 op_sel_hi:[0,0,0]
	v_mfma_scale_f32_16x16x128_f8f6f4 v[30:33], v[2:9], v[172:179], v[30:33], v232, v232 op_sel_hi:[0,0,0]
	v_mfma_scale_f32_16x16x128_f8f6f4 v[26:29], v[10:17], v[172:179], v[26:29], v232, v232 op_sel_hi:[0,0,0]
	v_mfma_scale_f32_16x16x128_f8f6f4 v[22:25], v[2:9], v[184:191], v[22:25], v232, v232 op_sel_hi:[0,0,0]
	v_mfma_scale_f32_16x16x128_f8f6f4 v[18:21], v[10:17], v[184:191], v[18:21], v232, v232 op_sel_hi:[0,0,0]
	s_setprio 0
	s_barrier
	ds_read_b128 v[2:5], v196
	ds_read_b128 v[6:9], v196 offset:1024
	ds_read_b128 v[10:13], v196 offset:2048
	ds_read_b128 v[14:17], v196 offset:3072
	s_add_u32 s6, s24, 0x10180
	s_addc_u32 s7, s25, 0
	s_mov_b32 m0, s4
	ds_read_b128 v[84:87], v183
	ds_read_b128 v[88:91], v183 offset:1024
	ds_read_b128 v[164:167], v183 offset:2048
	ds_read_b128 v[168:171], v183 offset:3072
	ds_read_b128 v[172:175], v183 offset:4096
	ds_read_b128 v[176:179], v183 offset:5120
	ds_read_b128 v[184:187], v183 offset:6144
	ds_read_b128 v[188:191], v183 offset:7168
	global_load_lds_dwordx4 v218, s[6:7]
	s_mov_b32 m0, s5
	s_nop 0
	global_load_lds_dwordx4 v96, s[6:7]
	s_waitcnt vmcnt(6)
	s_waitcnt lgkmcnt(0)
	s_barrier
	s_setprio 1
	v_mfma_scale_f32_16x16x128_f8f6f4 v[78:81], v[2:9], v[84:91], v[78:81], v232, v232 op_sel_hi:[0,0,0]
	v_mfma_scale_f32_16x16x128_f8f6f4 v[74:77], v[10:17], v[84:91], v[74:77], v232, v232 op_sel_hi:[0,0,0]
	v_mfma_scale_f32_16x16x128_f8f6f4 v[70:73], v[2:9], v[164:171], v[70:73], v232, v232 op_sel_hi:[0,0,0]
	v_mfma_scale_f32_16x16x128_f8f6f4 v[66:69], v[10:17], v[164:171], v[66:69], v232, v232 op_sel_hi:[0,0,0]
	v_mfma_scale_f32_16x16x128_f8f6f4 v[62:65], v[2:9], v[172:179], v[62:65], v232, v232 op_sel_hi:[0,0,0]
	v_mfma_scale_f32_16x16x128_f8f6f4 v[58:61], v[10:17], v[172:179], v[58:61], v232, v232 op_sel_hi:[0,0,0]
	v_mfma_scale_f32_16x16x128_f8f6f4 v[54:57], v[2:9], v[184:191], v[54:57], v232, v232 op_sel_hi:[0,0,0]
	v_mfma_scale_f32_16x16x128_f8f6f4 v[50:53], v[10:17], v[184:191], v[50:53], v232, v232 op_sel_hi:[0,0,0]
	s_setprio 0
	s_barrier
	s_mul_i32 s4, s19, s28
	s_mul_hi_i32 s5, s19, s28
	s_add_u32 s4, s4, s29
	s_addc_u32 s5, s5, s60
	v_cmp_gt_i64_e32 vcc, s[4:5], v[252:253]
	v_cmp_lt_i64_e64 s[6:7], s[4:5], v[220:221]
	s_cbranch_vccnz .LBB0_878
	s_ashr_i32 s15, s4, 31
	s_lshr_b32 s15, s15, 29
	s_add_i32 s15, s4, s15
	s_ashr_i32 s16, s15, 3
	s_and_b32 s15, s15, -8
	s_sub_i32 s4, s4, s15
	s_lshr_b32 s15, s4, 31
	s_or_b32 s15, s15, 32
	s_mul_i32 s4, s15, s4
	s_add_i32 s16, s4, s16
	s_ashr_i32 s4, s16, 31
	s_lshr_b32 s4, s4, 27
	s_add_i32 s17, s16, s4
	s_mul_i32 s19, s19, 6
	s_ashr_i32 s4, s17, 5
	s_sub_i32 s5, s61, s19
	s_lshl_b32 s19, s4, 3
	s_sub_i32 s4, 64, s19
	s_min_i32 s20, s4, 8
	s_abs_i32 s21, s20
	v_cvt_f32_u32_e32 v83, s21
	s_mul_hi_u32 s14, s5, 0x55555556
	s_lshl_b32 s18, s14, 7
	s_mul_i32 s14, s14, -3
	v_rcp_iflag_f32_e32 v83, v83
	s_add_i32 s14, s5, s14
	s_sub_i32 s36, 0, s21
	s_ashr_i32 s15, s14, 31
	v_mul_f32_e32 v83, 0x4f7ffffe, v83
	v_cvt_u32_f32_e32 v83, v83
	s_andn2_b32 s17, s17, 31
	s_lshl_b64 s[4:5], s[14:15], 19
	s_sub_i32 s15, s16, s17
	v_readfirstlane_b32 s38, v83
	s_mul_i32 s36, s36, s38
	s_mul_hi_u32 s36, s38, s36
	s_abs_i32 s17, s15
	s_add_i32 s38, s38, s36
	s_mul_hi_u32 s36, s17, s38
	s_mul_i32 s38, s36, s21
	s_xor_b32 s16, s15, s20
	s_sub_i32 s17, s17, s38
	s_ashr_i32 s16, s16, 31
	s_add_i32 s38, s36, 1
	s_sub_i32 s52, s17, s21
	s_cmp_ge_u32 s17, s21
	s_cselect_b32 s36, s38, s36
	s_cselect_b32 s17, s52, s17
	s_add_i32 s38, s36, 1
	s_cmp_ge_u32 s17, s21
	s_cselect_b32 s17, s38, s36
	s_xor_b32 s17, s17, s16
	s_sub_i32 s21, s17, s16
	s_mul_i32 s16, s21, s20
	s_sub_i32 s15, s15, s16
	s_add_i32 s15, s15, s19
	s_cmp_gt_i32 s15, 31
	s_cselect_b32 s16, 2, 1
	s_add_i32 s52, s16, s15
	s_mul_i32 s16, s14, 0x1100000
	s_mul_hi_i32 s15, s14, 0x1100000
	s_add_u32 s19, s30, s16
	s_addc_u32 s15, s31, s15
	s_ashr_i32 s53, s52, 31
	s_lshl_b64 s[16:17], s[52:53], 17
	s_add_u32 s16, s19, s16
	s_addc_u32 s17, s15, s17
	s_add_u32 s15, s34, s4
	s_addc_u32 s36, s35, s5
	s_lshl_b32 s4, s21, 8
	s_add_i32 s18, s4, s18
	s_ashr_i32 s19, s18, 31
	s_lshl_b64 s[4:5], s[18:19], 9
	s_add_u32 s20, s15, s4
	s_mov_b32 s97, 0x100000
	s_addc_u32 s21, s36, s5
	s_lshl_b32 s15, s52, 8
	s_movk_i32 s96, 0x1000

.LBB0_880:
	s_mov_b32 m0, s40
	v_lshl_add_u64 v[92:93], s[26:27], 0, v[94:95]
	ds_read_b128 v[84:87], v183 offset:16384
	ds_read_b128 v[88:91], v183 offset:17408
	ds_read_b128 v[164:167], v183 offset:18432
	ds_read_b128 v[168:171], v183 offset:19456
	ds_read_b128 v[172:175], v183 offset:20480
	ds_read_b128 v[176:179], v183 offset:21504
	ds_read_b128 v[184:187], v183 offset:22528
	ds_read_b128 v[188:191], v183 offset:23552
	global_load_lds_dwordx4 v[92:93], off
	v_lshl_add_u64 v[180:181], s[26:27], 0, v[98:99]
	s_mov_b32 m0, s41
	v_lshl_add_u64 v[192:193], s[24:25], 0, v[218:219]
	global_load_lds_dwordx4 v[180:181], off
	v_lshl_add_u64 v[194:195], s[24:25], 0, v[96:97]
	s_add_u32 s6, s24, 0x10000
	s_mov_b32 m0, s44
	s_addc_u32 s7, s25, 0
	global_load_lds_dwordx4 v[192:193], off
	s_mov_b32 m0, s45
	s_nop 0
	global_load_lds_dwordx4 v[194:195], off
	s_waitcnt vmcnt(6)
	s_waitcnt lgkmcnt(0)
	s_barrier
	s_setprio 1
	v_mfma_scale_f32_16x16x128_f8f6f4 v[46:49], v[2:9], v[84:91], v[46:49], v232, v232 op_sel_hi:[0,0,0]
	v_mfma_scale_f32_16x16x128_f8f6f4 v[42:45], v[10:17], v[84:91], v[42:45], v232, v232 op_sel_hi:[0,0,0]
	v_mfma_scale_f32_16x16x128_f8f6f4 v[38:41], v[2:9], v[164:171], v[38:41], v232, v232 op_sel_hi:[0,0,0]
	v_mfma_scale_f32_16x16x128_f8f6f4 v[34:37], v[10:17], v[164:171], v[34:37], v232, v232 op_sel_hi:[0,0,0]
	v_mfma_scale_f32_16x16x128_f8f6f4 v[30:33], v[2:9], v[172:179], v[30:33], v232, v232 op_sel_hi:[0,0,0]
	v_mfma_scale_f32_16x16x128_f8f6f4 v[26:29], v[10:17], v[172:179], v[26:29], v232, v232 op_sel_hi:[0,0,0]
	v_mfma_scale_f32_16x16x128_f8f6f4 v[22:25], v[2:9], v[184:191], v[22:25], v232, v232 op_sel_hi:[0,0,0]
	v_mfma_scale_f32_16x16x128_f8f6f4 v[18:21], v[10:17], v[184:191], v[18:21], v232, v232 op_sel_hi:[0,0,0]
	s_setprio 0
	s_barrier
	ds_read_b128 v[2:5], v82
	ds_read_b128 v[6:9], v82 offset:1024
	ds_read_b128 v[10:13], v82 offset:2048
	ds_read_b128 v[14:17], v82 offset:3072
	s_mov_b32 m0, s46
	v_lshl_add_u64 v[90:91], s[6:7], 0, v[218:219]
	ds_read_b128 v[82:85], v183 offset:32768
	ds_read_b128 v[86:89], v183 offset:33792
	ds_read_b128 v[164:167], v183 offset:34816
	ds_read_b128 v[168:171], v183 offset:35840
	ds_read_b128 v[172:175], v183 offset:36864
	ds_read_b128 v[176:179], v183 offset:37888
	ds_read_b128 v[184:187], v183 offset:38912
	ds_read_b128 v[188:191], v183 offset:39936
	global_load_lds_dwordx4 v[90:91], off
	s_mov_b32 m0, s47
	v_lshl_add_u64 v[90:91], s[6:7], 0, v[96:97]
	global_load_lds_dwordx4 v[90:91], off
	s_waitcnt vmcnt(6)
	s_waitcnt lgkmcnt(0)
	s_barrier
	s_setprio 1
	v_mfma_scale_f32_16x16x128_f8f6f4 v[78:81], v[2:9], v[82:89], v[78:81], v232, v232 op_sel_hi:[0,0,0]
	v_mfma_scale_f32_16x16x128_f8f6f4 v[74:77], v[10:17], v[82:89], v[74:77], v232, v232 op_sel_hi:[0,0,0]
	v_mfma_scale_f32_16x16x128_f8f6f4 v[70:73], v[2:9], v[164:171], v[70:73], v232, v232 op_sel_hi:[0,0,0]
	v_mfma_scale_f32_16x16x128_f8f6f4 v[66:69], v[10:17], v[164:171], v[66:69], v232, v232 op_sel_hi:[0,0,0]
	v_mfma_scale_f32_16x16x128_f8f6f4 v[62:65], v[2:9], v[172:179], v[62:65], v232, v232 op_sel_hi:[0,0,0]
	v_mfma_scale_f32_16x16x128_f8f6f4 v[58:61], v[10:17], v[172:179], v[58:61], v232, v232 op_sel_hi:[0,0,0]
	v_mfma_scale_f32_16x16x128_f8f6f4 v[54:57], v[2:9], v[184:191], v[54:57], v232, v232 op_sel_hi:[0,0,0]
	v_mfma_scale_f32_16x16x128_f8f6f4 v[50:53], v[10:17], v[184:191], v[50:53], v232, v232 op_sel_hi:[0,0,0]
	s_setprio 0
	s_barrier
	s_mov_b32 m0, s49
	v_lshl_add_u64 v[90:91], v[92:93], 0, s[72:73]
	ds_read_b128 v[82:85], v183 offset:49152
	ds_read_b128 v[86:89], v183 offset:50176
	ds_read_b128 v[164:167], v183 offset:51200
	ds_read_b128 v[168:171], v183 offset:52224
	ds_read_b128 v[172:175], v183 offset:53248
	ds_read_b128 v[176:179], v183 offset:54272
	ds_read_b128 v[184:187], v183 offset:55296
	ds_read_b128 v[188:191], v183 offset:56320
	global_load_lds_dwordx4 v[90:91], off
	s_mov_b32 m0, s50
	v_lshl_add_u64 v[92:93], v[180:181], 0, s[72:73]
	global_load_lds_dwordx4 v[92:93], off
	s_nop 0
	s_mov_b32 m0, s51
	v_lshl_add_u64 v[90:91], v[192:193], 0, s[72:73]
	global_load_lds_dwordx4 v[90:91], off
	s_mov_b32 m0, s56
	v_lshl_add_u64 v[90:91], v[194:195], 0, s[72:73]
	global_load_lds_dwordx4 v[90:91], off
	s_waitcnt vmcnt(6)
	s_waitcnt lgkmcnt(0)
	s_barrier
	s_setprio 1
	v_mfma_scale_f32_16x16x128_f8f6f4 v[46:49], v[2:9], v[82:89], v[46:49], v232, v232 op_sel_hi:[0,0,0]
	v_mfma_scale_f32_16x16x128_f8f6f4 v[42:45], v[10:17], v[82:89], v[42:45], v232, v232 op_sel_hi:[0,0,0]
	v_mfma_scale_f32_16x16x128_f8f6f4 v[38:41], v[2:9], v[164:171], v[38:41], v232, v232 op_sel_hi:[0,0,0]
	v_mfma_scale_f32_16x16x128_f8f6f4 v[34:37], v[10:17], v[164:171], v[34:37], v232, v232 op_sel_hi:[0,0,0]
	v_mfma_scale_f32_16x16x128_f8f6f4 v[30:33], v[2:9], v[172:179], v[30:33], v232, v232 op_sel_hi:[0,0,0]
	v_mfma_scale_f32_16x16x128_f8f6f4 v[26:29], v[10:17], v[172:179], v[26:29], v232, v232 op_sel_hi:[0,0,0]
	v_mfma_scale_f32_16x16x128_f8f6f4 v[22:25], v[2:9], v[184:191], v[22:25], v232, v232 op_sel_hi:[0,0,0]
	v_mfma_scale_f32_16x16x128_f8f6f4 v[18:21], v[10:17], v[184:191], v[18:21], v232, v232 op_sel_hi:[0,0,0]
	s_setprio 0
	s_barrier
	s_andn2_b64 vcc, exec, s[12:13]
	s_cbranch_vccnz .LBB0_882
	s_barrier

.LBB0_1008:
	s_mov_b32 m0, s45
	ds_read_b128 v[174:177], v173 offset:16384
	ds_read_b128 v[178:181], v173 offset:17408
	ds_read_b128 v[182:185], v173 offset:18432
	ds_read_b128 v[186:189], v173 offset:19456
	ds_read_b128 v[190:193], v173 offset:20480
	ds_read_b128 v[194:197], v173 offset:21504
	ds_read_b128 v[198:201], v173 offset:22528
	ds_read_b128 v[202:205], v173 offset:23552
	global_load_lds_dwordx4 v164, s[60:61]
	s_mov_b32 m0, s46
	v_lshl_add_u64 v[212:213], s[34:35], 0, v[218:219]
	global_load_lds_dwordx4 v168, s[60:61]
	s_mov_b32 m0, s48
	v_lshl_add_u64 v[214:215], s[34:35], 0, v[166:167]
	global_load_lds_dwordx4 v164, s[56:57]
	s_mov_b32 m0, s49
	v_mov_b32_e32 v165, v219
	global_load_lds_dwordx4 v168, s[56:57]
	s_mov_b32 m0, s50
	v_mov_b32_e32 v169, v219
	global_load_lds_dwordx4 v[212:213], off
	s_mov_b32 m0, s51
	v_lshl_add_u64 v[170:171], s[60:61], 0, v[164:165]
	global_load_lds_dwordx4 v[214:215], off
	s_waitcnt vmcnt(8)
	s_waitcnt lgkmcnt(0)
	v_lshl_add_u64 v[206:207], s[60:61], 0, v[168:169]
	v_lshl_add_u64 v[208:209], s[56:57], 0, v[164:165]
	v_lshl_add_u64 v[210:211], s[56:57], 0, v[168:169]
	s_barrier
	s_setprio 1
	s_waitcnt lgkmcnt(0)
	v_mfma_f32_16x16x32_bf16 v[62:65], v[146:149], v[174:177], v[62:65]
	v_mfma_f32_16x16x32_bf16 v[58:61], v[154:157], v[174:177], v[58:61]
	v_mfma_f32_16x16x32_bf16 v[54:57], v[146:149], v[182:185], v[54:57]
	v_mfma_f32_16x16x32_bf16 v[50:53], v[154:157], v[182:185], v[50:53]
	v_mfma_f32_16x16x32_bf16 v[46:49], v[146:149], v[190:193], v[46:49]
	v_mfma_f32_16x16x32_bf16 v[42:45], v[154:157], v[190:193], v[42:45]
	v_mfma_f32_16x16x32_bf16 v[38:41], v[146:149], v[198:201], v[38:41]
	v_mfma_f32_16x16x32_bf16 v[34:37], v[154:157], v[198:201], v[34:37]
	v_mfma_f32_16x16x32_bf16 v[62:65], v[150:153], v[178:181], v[62:65]
	v_mfma_f32_16x16x32_bf16 v[58:61], v[158:161], v[178:181], v[58:61]
	v_mfma_f32_16x16x32_bf16 v[54:57], v[150:153], v[186:189], v[54:57]
	v_mfma_f32_16x16x32_bf16 v[50:53], v[158:161], v[186:189], v[50:53]
	v_mfma_f32_16x16x32_bf16 v[46:49], v[150:153], v[194:197], v[46:49]
	v_mfma_f32_16x16x32_bf16 v[42:45], v[158:161], v[194:197], v[42:45]
	v_mfma_f32_16x16x32_bf16 v[38:41], v[150:153], v[202:205], v[38:41]
	v_mfma_f32_16x16x32_bf16 v[34:37], v[158:161], v[202:205], v[34:37]
	v_mfma_f32_16x16x32_bf16 v[30:33], v[130:133], v[174:177], v[30:33]
	v_mfma_f32_16x16x32_bf16 v[26:29], v[138:141], v[174:177], v[26:29]
	v_mfma_f32_16x16x32_bf16 v[22:25], v[130:133], v[182:185], v[22:25]
	v_mfma_f32_16x16x32_bf16 v[18:21], v[138:141], v[182:185], v[18:21]
	v_mfma_f32_16x16x32_bf16 v[14:17], v[130:133], v[190:193], v[14:17]
	v_mfma_f32_16x16x32_bf16 v[10:13], v[138:141], v[190:193], v[10:13]
	v_mfma_f32_16x16x32_bf16 v[6:9], v[130:133], v[198:201], v[6:9]
	v_mfma_f32_16x16x32_bf16 v[2:5], v[138:141], v[198:201], v[2:5]
	v_mfma_f32_16x16x32_bf16 v[30:33], v[134:137], v[178:181], v[30:33]
	v_mfma_f32_16x16x32_bf16 v[26:29], v[142:145], v[178:181], v[26:29]
	v_mfma_f32_16x16x32_bf16 v[22:25], v[134:137], v[186:189], v[22:25]
	v_mfma_f32_16x16x32_bf16 v[18:21], v[142:145], v[186:189], v[18:21]
	v_mfma_f32_16x16x32_bf16 v[14:17], v[134:137], v[194:197], v[14:17]
	v_mfma_f32_16x16x32_bf16 v[10:13], v[142:145], v[194:197], v[10:13]
	v_mfma_f32_16x16x32_bf16 v[6:9], v[134:137], v[202:205], v[6:9]
	v_mfma_f32_16x16x32_bf16 v[2:5], v[142:145], v[202:205], v[2:5]
	s_setprio 0
	s_barrier
	v_add_u32_e32 v142, s58, v172
	v_add_u32_e32 v158, s80, v172
	ds_read_b128 v[130:133], v142
	ds_read_b128 v[134:137], v142 offset:1024
	ds_read_b128 v[138:141], v142 offset:2048
	ds_read_b128 v[142:145], v142 offset:3072
	ds_read_b128 v[146:149], v158
	ds_read_b128 v[150:153], v158 offset:1024
	ds_read_b128 v[154:157], v158 offset:2048
	ds_read_b128 v[158:161], v158 offset:3072
	s_mov_b32 m0, s52
	v_lshl_add_u64 v[216:217], s[6:7], 0, v[218:219]
	ds_read_b128 v[174:177], v173 offset:32768
	ds_read_b128 v[178:181], v173 offset:33792
	ds_read_b128 v[182:185], v173 offset:34816
	ds_read_b128 v[186:189], v173 offset:35840
	ds_read_b128 v[190:193], v173 offset:36864
	ds_read_b128 v[194:197], v173 offset:37888
	ds_read_b128 v[198:201], v173 offset:38912
	ds_read_b128 v[202:205], v173 offset:39936
	global_load_lds_dwordx4 v[216:217], off
	s_mov_b32 m0, s53
	v_lshl_add_u64 v[216:217], s[6:7], 0, v[166:167]
	global_load_lds_dwordx4 v[216:217], off
	s_waitcnt vmcnt(8)
	s_waitcnt lgkmcnt(0)
	s_barrier
	s_setprio 1
	v_mfma_f32_16x16x32_bf16 v[126:129], v[130:133], v[174:177], v[126:129]
	v_mfma_f32_16x16x32_bf16 v[122:125], v[138:141], v[174:177], v[122:125]
	v_mfma_f32_16x16x32_bf16 v[118:121], v[130:133], v[182:185], v[118:121]
	v_mfma_f32_16x16x32_bf16 v[114:117], v[138:141], v[182:185], v[114:117]
	v_mfma_f32_16x16x32_bf16 v[110:113], v[130:133], v[190:193], v[110:113]
	v_mfma_f32_16x16x32_bf16 v[106:109], v[138:141], v[190:193], v[106:109]
	v_mfma_f32_16x16x32_bf16 v[102:105], v[130:133], v[198:201], v[102:105]
	v_mfma_f32_16x16x32_bf16 v[98:101], v[138:141], v[198:201], v[98:101]
	v_mfma_f32_16x16x32_bf16 v[126:129], v[134:137], v[178:181], v[126:129]
	v_mfma_f32_16x16x32_bf16 v[122:125], v[142:145], v[178:181], v[122:125]
	v_mfma_f32_16x16x32_bf16 v[118:121], v[134:137], v[186:189], v[118:121]
	v_mfma_f32_16x16x32_bf16 v[114:117], v[142:145], v[186:189], v[114:117]
	v_mfma_f32_16x16x32_bf16 v[110:113], v[134:137], v[194:197], v[110:113]
	v_mfma_f32_16x16x32_bf16 v[106:109], v[142:145], v[194:197], v[106:109]
	v_mfma_f32_16x16x32_bf16 v[102:105], v[134:137], v[202:205], v[102:105]
	v_mfma_f32_16x16x32_bf16 v[98:101], v[142:145], v[202:205], v[98:101]
	v_mfma_f32_16x16x32_bf16 v[94:97], v[146:149], v[174:177], v[94:97]
	v_mfma_f32_16x16x32_bf16 v[90:93], v[154:157], v[174:177], v[90:93]
	v_mfma_f32_16x16x32_bf16 v[86:89], v[146:149], v[182:185], v[86:89]
	v_mfma_f32_16x16x32_bf16 v[82:85], v[154:157], v[182:185], v[82:85]
	v_mfma_f32_16x16x32_bf16 v[78:81], v[146:149], v[190:193], v[78:81]
	v_mfma_f32_16x16x32_bf16 v[74:77], v[154:157], v[190:193], v[74:77]
	v_mfma_f32_16x16x32_bf16 v[70:73], v[146:149], v[198:201], v[70:73]
	v_mfma_f32_16x16x32_bf16 v[66:69], v[154:157], v[198:201], v[66:69]
	v_mfma_f32_16x16x32_bf16 v[94:97], v[150:153], v[178:181], v[94:97]
	v_mfma_f32_16x16x32_bf16 v[90:93], v[158:161], v[178:181], v[90:93]
	v_mfma_f32_16x16x32_bf16 v[86:89], v[150:153], v[186:189], v[86:89]
	v_mfma_f32_16x16x32_bf16 v[82:85], v[158:161], v[186:189], v[82:85]
	v_mfma_f32_16x16x32_bf16 v[78:81], v[150:153], v[194:197], v[78:81]
	v_mfma_f32_16x16x32_bf16 v[74:77], v[158:161], v[194:197], v[74:77]
	v_mfma_f32_16x16x32_bf16 v[70:73], v[150:153], v[202:205], v[70:73]
	v_mfma_f32_16x16x32_bf16 v[66:69], v[158:161], v[202:205], v[66:69]
	s_setprio 0
	s_barrier
	s_mov_b32 m0, s66
	v_lshl_add_u64 v[170:171], v[170:171], 0, s[72:73]
	ds_read_b128 v[174:177], v173 offset:49152
	ds_read_b128 v[178:181], v173 offset:50176
	ds_read_b128 v[182:185], v173 offset:51200
	ds_read_b128 v[186:189], v173 offset:52224
	ds_read_b128 v[190:193], v173 offset:53248
	ds_read_b128 v[194:197], v173 offset:54272
	ds_read_b128 v[198:201], v173 offset:55296
	ds_read_b128 v[202:205], v173 offset:56320
	global_load_lds_dwordx4 v[170:171], off
	s_mov_b32 m0, s67
	v_lshl_add_u64 v[170:171], v[206:207], 0, s[72:73]
	global_load_lds_dwordx4 v[170:171], off
	s_mov_b32 m0, s81
	v_lshl_add_u64 v[170:171], v[208:209], 0, s[72:73]
	global_load_lds_dwordx4 v[170:171], off
	s_mov_b32 m0, s82
	v_lshl_add_u64 v[170:171], v[210:211], 0, s[72:73]
	global_load_lds_dwordx4 v[170:171], off
	s_mov_b32 m0, s70
	v_lshl_add_u64 v[170:171], v[212:213], 0, s[72:73]
	global_load_lds_dwordx4 v[170:171], off
	s_mov_b32 m0, s71
	v_lshl_add_u64 v[170:171], v[214:215], 0, s[72:73]
	global_load_lds_dwordx4 v[170:171], off
	s_waitcnt vmcnt(8)
	s_waitcnt lgkmcnt(0)
	s_barrier
	s_setprio 1
	v_mfma_f32_16x16x32_bf16 v[62:65], v[130:133], v[174:177], v[62:65]
	v_mfma_f32_16x16x32_bf16 v[58:61], v[138:141], v[174:177], v[58:61]
	v_mfma_f32_16x16x32_bf16 v[54:57], v[130:133], v[182:185], v[54:57]
	v_mfma_f32_16x16x32_bf16 v[50:53], v[138:141], v[182:185], v[50:53]
	v_mfma_f32_16x16x32_bf16 v[46:49], v[130:133], v[190:193], v[46:49]
	v_mfma_f32_16x16x32_bf16 v[42:45], v[138:141], v[190:193], v[42:45]
	v_mfma_f32_16x16x32_bf16 v[38:41], v[130:133], v[198:201], v[38:41]
	v_mfma_f32_16x16x32_bf16 v[34:37], v[138:141], v[198:201], v[34:37]
	v_mfma_f32_16x16x32_bf16 v[62:65], v[134:137], v[178:181], v[62:65]
	v_mfma_f32_16x16x32_bf16 v[58:61], v[142:145], v[178:181], v[58:61]
	v_mfma_f32_16x16x32_bf16 v[54:57], v[134:137], v[186:189], v[54:57]
	v_mfma_f32_16x16x32_bf16 v[50:53], v[142:145], v[186:189], v[50:53]
	v_mfma_f32_16x16x32_bf16 v[46:49], v[134:137], v[194:197], v[46:49]
	v_mfma_f32_16x16x32_bf16 v[42:45], v[142:145], v[194:197], v[42:45]
	v_mfma_f32_16x16x32_bf16 v[38:41], v[134:137], v[202:205], v[38:41]
	v_mfma_f32_16x16x32_bf16 v[34:37], v[142:145], v[202:205], v[34:37]
	v_mfma_f32_16x16x32_bf16 v[30:33], v[146:149], v[174:177], v[30:33]
	v_mfma_f32_16x16x32_bf16 v[26:29], v[154:157], v[174:177], v[26:29]
	v_mfma_f32_16x16x32_bf16 v[22:25], v[146:149], v[182:185], v[22:25]
	v_mfma_f32_16x16x32_bf16 v[18:21], v[154:157], v[182:185], v[18:21]
	v_mfma_f32_16x16x32_bf16 v[14:17], v[146:149], v[190:193], v[14:17]
	v_mfma_f32_16x16x32_bf16 v[10:13], v[154:157], v[190:193], v[10:13]
	v_mfma_f32_16x16x32_bf16 v[6:9], v[146:149], v[198:201], v[6:9]
	v_mfma_f32_16x16x32_bf16 v[2:5], v[154:157], v[198:201], v[2:5]
	v_mfma_f32_16x16x32_bf16 v[30:33], v[150:153], v[178:181], v[30:33]
	v_mfma_f32_16x16x32_bf16 v[26:29], v[158:161], v[178:181], v[26:29]
	v_mfma_f32_16x16x32_bf16 v[22:25], v[150:153], v[186:189], v[22:25]
	v_mfma_f32_16x16x32_bf16 v[18:21], v[158:161], v[186:189], v[18:21]
	v_mfma_f32_16x16x32_bf16 v[14:17], v[150:153], v[194:197], v[14:17]
	v_mfma_f32_16x16x32_bf16 v[10:13], v[158:161], v[194:197], v[10:13]
	v_mfma_f32_16x16x32_bf16 v[6:9], v[150:153], v[202:205], v[6:9]
	v_mfma_f32_16x16x32_bf16 v[2:5], v[158:161], v[202:205], v[2:5]
	s_setprio 0
	s_barrier
	s_add_i32 s91, s91, 2
	s_add_u32 s30, s30, 0x100
	s_addc_u32 s31, s31, 0
	s_cmp_gt_u32 s91, 13
	s_cbranch_scc1 .LBB0_1016
.LBB0_1009:
	v_add_u32_e32 v130, s38, v172
	v_add_u32_e32 v142, s47, v172
	ds_read_b128 v[146:149], v130
	ds_read_b128 v[150:153], v130 offset:1024
	ds_read_b128 v[154:157], v130 offset:2048
	ds_read_b128 v[158:161], v130 offset:3072
	ds_read_b128 v[130:133], v142
	ds_read_b128 v[134:137], v142 offset:1024
	ds_read_b128 v[138:141], v142 offset:2048
	ds_read_b128 v[142:145], v142 offset:3072
	s_add_u32 s6, s18, s30
	s_addc_u32 s7, s19, s31
	v_lshl_add_u64 v[170:171], s[6:7], 0, v[218:219]
	v_lshl_add_u64 v[170:171], v[170:171], 0, s[64:65]
	s_add_i32 m0, s50, 0xc000
	v_mov_b32_e32 v167, v219
	ds_read_b128 v[174:177], v173
	ds_read_b128 v[178:181], v173 offset:1024
	ds_read_b128 v[182:185], v173 offset:2048
	ds_read_b128 v[186:189], v173 offset:3072
	ds_read_b128 v[190:193], v173 offset:4096
	ds_read_b128 v[194:197], v173 offset:5120
	ds_read_b128 v[198:201], v173 offset:6144
	ds_read_b128 v[202:205], v173 offset:7168
	global_load_lds_dwordx4 v[170:171], off
	v_lshl_add_u64 v[170:171], s[6:7], 0, v[166:167]
	v_lshl_add_u64 v[170:171], v[170:171], 0, s[64:65]
	s_add_i32 m0, s50, 0xe000
	s_nop 0
	global_load_lds_dwordx4 v[170:171], off
	s_waitcnt vmcnt(8)
	s_waitcnt lgkmcnt(0)
	s_barrier
	s_setprio 1
	v_mfma_f32_16x16x32_bf16 v[126:129], v[146:149], v[174:177], v[126:129]
	v_mfma_f32_16x16x32_bf16 v[122:125], v[154:157], v[174:177], v[122:125]
	v_mfma_f32_16x16x32_bf16 v[118:121], v[146:149], v[182:185], v[118:121]
	v_mfma_f32_16x16x32_bf16 v[114:117], v[154:157], v[182:185], v[114:117]
	v_mfma_f32_16x16x32_bf16 v[110:113], v[146:149], v[190:193], v[110:113]
	v_mfma_f32_16x16x32_bf16 v[106:109], v[154:157], v[190:193], v[106:109]
	v_mfma_f32_16x16x32_bf16 v[102:105], v[146:149], v[198:201], v[102:105]
	v_mfma_f32_16x16x32_bf16 v[98:101], v[154:157], v[198:201], v[98:101]
	v_mfma_f32_16x16x32_bf16 v[126:129], v[150:153], v[178:181], v[126:129]
	v_mfma_f32_16x16x32_bf16 v[122:125], v[158:161], v[178:181], v[122:125]
	v_mfma_f32_16x16x32_bf16 v[118:121], v[150:153], v[186:189], v[118:121]
	v_mfma_f32_16x16x32_bf16 v[114:117], v[158:161], v[186:189], v[114:117]
	v_mfma_f32_16x16x32_bf16 v[110:113], v[150:153], v[194:197], v[110:113]
	v_mfma_f32_16x16x32_bf16 v[106:109], v[158:161], v[194:197], v[106:109]
	v_mfma_f32_16x16x32_bf16 v[102:105], v[150:153], v[202:205], v[102:105]
	v_mfma_f32_16x16x32_bf16 v[98:101], v[158:161], v[202:205], v[98:101]
	v_mfma_f32_16x16x32_bf16 v[94:97], v[130:133], v[174:177], v[94:97]
	s_cmpk_lg_i32 s30, 0x700
	v_mfma_f32_16x16x32_bf16 v[90:93], v[138:141], v[174:177], v[90:93]
	v_mfma_f32_16x16x32_bf16 v[86:89], v[130:133], v[182:185], v[86:89]
	v_mfma_f32_16x16x32_bf16 v[82:85], v[138:141], v[182:185], v[82:85]
	v_mfma_f32_16x16x32_bf16 v[78:81], v[130:133], v[190:193], v[78:81]
	v_mfma_f32_16x16x32_bf16 v[74:77], v[138:141], v[190:193], v[74:77]
	v_mfma_f32_16x16x32_bf16 v[70:73], v[130:133], v[198:201], v[70:73]
	v_mfma_f32_16x16x32_bf16 v[66:69], v[138:141], v[198:201], v[66:69]
	v_mfma_f32_16x16x32_bf16 v[94:97], v[134:137], v[178:181], v[94:97]
	v_mfma_f32_16x16x32_bf16 v[90:93], v[142:145], v[178:181], v[90:93]
	v_mfma_f32_16x16x32_bf16 v[86:89], v[134:137], v[186:189], v[86:89]
	v_mfma_f32_16x16x32_bf16 v[82:85], v[142:145], v[186:189], v[82:85]
	v_mfma_f32_16x16x32_bf16 v[78:81], v[134:137], v[194:197], v[78:81]
	v_mfma_f32_16x16x32_bf16 v[74:77], v[142:145], v[194:197], v[74:77]
	v_mfma_f32_16x16x32_bf16 v[70:73], v[134:137], v[202:205], v[70:73]
	v_mfma_f32_16x16x32_bf16 v[66:69], v[142:145], v[202:205], v[66:69]
	s_setprio 0
	s_barrier
	s_mov_b64 s[62:63], -1
	s_cbranch_scc0 .LBB0_1011
	s_add_u32 s6, s18, s30
	s_addc_u32 s7, s19, s31
	s_add_u32 s34, s6, 0x100
	s_addc_u32 s35, s7, 0
	s_add_u32 s56, s20, s30
	s_addc_u32 s57, s21, s31
	s_add_u32 s60, s56, 0x100
	s_addc_u32 s61, s57, 0
	s_add_u32 s6, s6, 0x40100
	s_addc_u32 s7, s7, 0
	s_add_u32 s56, s56, 0x40100
	s_addc_u32 s57, s57, 0
	s_mov_b64 s[62:63], 0

.LBB0_1260:
	s_andn2_b64 vcc, exec, s[2:3]
	s_cbranch_vccnz .LBB0_1262
	s_mov_b32 m0, s38
	v_lshl_add_u64 v[2:3], s[18:19], 0, v[162:163]
	global_load_lds_dwordx4 v[2:3], off
.LBB0_1262:
	v_add_u32_e32 v18, s27, v190
	v_add_u32_e32 v22, s43, v190
	ds_read_b128 v[10:13], v18
	ds_read_b128 v[14:17], v18 offset:1024
	ds_read_b128 v[24:27], v18 offset:2048
	ds_read_b128 v[28:31], v18 offset:3072
	ds_read_b128 v[182:185], v22
	ds_read_b128 v[186:189], v22 offset:1024
	ds_read_b128 v[192:195], v22 offset:2048
	ds_read_b128 v[196:199], v22 offset:3072
	s_add_i32 s94, s33, 1
	v_lshl_add_u64 v[178:179], s[6:7], 0, v[218:219]
	s_add_i32 s31, s46, 0xc000
	v_mov_b32_e32 v173, v219
	v_lshl_add_u64 v[20:21], v[178:179], 0, s[72:73]
	s_mov_b32 m0, s31
	v_lshl_add_u64 v[180:181], s[6:7], 0, v[172:173]
	s_add_i32 s30, s46, 0xe000
	ds_read_b128 v[2:5], v191
	ds_read_b128 v[6:9], v191 offset:1024
	ds_read_b128 v[38:41], v191 offset:2048
	ds_read_b128 v[42:45], v191 offset:3072
	ds_read_b128 v[46:49], v191 offset:4096
	ds_read_b128 v[50:53], v191 offset:5120
	ds_read_b128 v[54:57], v191 offset:6144
	ds_read_b128 v[58:61], v191 offset:7168
	global_load_lds_dwordx4 v[20:21], off
	s_mov_b32 m0, s30
	v_lshl_add_u64 v[20:21], v[180:181], 0, s[72:73]
	global_load_lds_dwordx4 v[20:21], off
	s_waitcnt vmcnt(8)
	s_waitcnt lgkmcnt(0)
	s_barrier
	s_setprio 1
	v_readlane_b32 s52, v255, 26
	v_readlane_b32 s53, v255, 27
	v_readlane_b32 s54, v255, 28
	v_readlane_b32 s55, v255, 29
	v_mov_b64_e32 v[34:35], s[52:53]
	s_nop 0
	v_mov_b64_e32 v[156:157], s[54:55]
	v_mov_b64_e32 v[148:149], s[54:55]
	v_mov_b64_e32 v[140:141], s[54:55]
	v_mov_b64_e32 v[132:133], s[54:55]
	v_mov_b64_e32 v[124:125], s[54:55]
	v_mov_b64_e32 v[116:117], s[54:55]
	v_mov_b64_e32 v[108:109], s[54:55]
	v_mov_b64_e32 v[100:101], s[54:55]
	v_mov_b64_e32 v[36:37], s[54:55]
	v_mov_b64_e32 v[154:155], s[52:53]
	v_mov_b64_e32 v[146:147], s[52:53]
	v_mov_b64_e32 v[138:139], s[52:53]
	v_mov_b64_e32 v[130:131], s[52:53]
	v_mov_b64_e32 v[122:123], s[52:53]
	v_mov_b64_e32 v[114:115], s[52:53]
	v_mov_b64_e32 v[106:107], s[52:53]
	v_mov_b64_e32 v[98:99], s[52:53]
	s_waitcnt lgkmcnt(0)
	v_mfma_scale_f32_16x16x128_f8f6f4 v[154:157], v[10:17], v[2:9], v[154:157], v232, v232 op_sel_hi:[0,0,0]
	v_mfma_scale_f32_16x16x128_f8f6f4 v[146:149], v[24:31], v[2:9], v[146:149], v232, v232 op_sel_hi:[0,0,0]
	v_mfma_scale_f32_16x16x128_f8f6f4 v[138:141], v[10:17], v[38:45], v[138:141], v232, v232 op_sel_hi:[0,0,0]
	v_mfma_scale_f32_16x16x128_f8f6f4 v[130:133], v[24:31], v[38:45], v[130:133], v232, v232 op_sel_hi:[0,0,0]
	v_mfma_scale_f32_16x16x128_f8f6f4 v[122:125], v[10:17], v[46:53], v[122:125], v232, v232 op_sel_hi:[0,0,0]
	v_mfma_scale_f32_16x16x128_f8f6f4 v[114:117], v[24:31], v[46:53], v[114:117], v232, v232 op_sel_hi:[0,0,0]
	v_mfma_scale_f32_16x16x128_f8f6f4 v[106:109], v[10:17], v[54:61], v[106:109], v232, v232 op_sel_hi:[0,0,0]
	v_mfma_scale_f32_16x16x128_f8f6f4 v[98:101], v[24:31], v[54:61], v[98:101], v232, v232 op_sel_hi:[0,0,0]
	v_mov_b64_e32 v[160:161], s[54:55]
	v_mov_b64_e32 v[152:153], s[54:55]
	v_mov_b64_e32 v[144:145], s[54:55]
	v_mov_b64_e32 v[136:137], s[54:55]
	v_mov_b64_e32 v[128:129], s[54:55]
	v_mov_b64_e32 v[120:121], s[54:55]
	v_mov_b64_e32 v[112:113], s[54:55]
	v_mov_b64_e32 v[104:105], s[54:55]
	v_mov_b64_e32 v[158:159], s[52:53]
	v_mov_b64_e32 v[150:151], s[52:53]
	v_mov_b64_e32 v[142:143], s[52:53]
	v_mov_b64_e32 v[134:135], s[52:53]
	v_mov_b64_e32 v[126:127], s[52:53]
	v_mov_b64_e32 v[118:119], s[52:53]
	v_mov_b64_e32 v[110:111], s[52:53]
	v_mov_b64_e32 v[102:103], s[52:53]
	v_mfma_scale_f32_16x16x128_f8f6f4 v[158:161], v[182:189], v[2:9], v[158:161], v232, v232 op_sel_hi:[0,0,0]
	v_mfma_scale_f32_16x16x128_f8f6f4 v[150:153], v[192:199], v[2:9], v[150:153], v232, v232 op_sel_hi:[0,0,0]
	v_mfma_scale_f32_16x16x128_f8f6f4 v[142:145], v[182:189], v[38:45], v[142:145], v232, v232 op_sel_hi:[0,0,0]
	v_mfma_scale_f32_16x16x128_f8f6f4 v[134:137], v[192:199], v[38:45], v[134:137], v232, v232 op_sel_hi:[0,0,0]
	v_mfma_scale_f32_16x16x128_f8f6f4 v[126:129], v[182:189], v[46:53], v[126:129], v232, v232 op_sel_hi:[0,0,0]
	v_mfma_scale_f32_16x16x128_f8f6f4 v[118:121], v[192:199], v[46:53], v[118:121], v232, v232 op_sel_hi:[0,0,0]
	v_mfma_scale_f32_16x16x128_f8f6f4 v[110:113], v[182:189], v[54:61], v[110:113], v232, v232 op_sel_hi:[0,0,0]
	v_mfma_scale_f32_16x16x128_f8f6f4 v[102:105], v[192:199], v[54:61], v[102:105], v232, v232 op_sel_hi:[0,0,0]
	s_setprio 0
	s_barrier
	v_mov_b32_e32 v165, v219
	v_lshl_add_u64 v[2:3], s[28:29], 0, v[164:165]
	s_mov_b32 m0, s41
	v_lshl_add_u64 v[4:5], v[2:3], 0, s[76:77]
	v_mov_b32_e32 v175, v219
	ds_read_b128 v[200:203], v191 offset:16384
	ds_read_b128 v[204:207], v191 offset:17408
	ds_read_b128 v[208:211], v191 offset:18432
	ds_read_b128 v[212:215], v191 offset:19456
	ds_read_b128 v[222:225], v191 offset:20480
	ds_read_b128 v[226:229], v191 offset:21504
	ds_read_b128 v[244:247], v191 offset:22528
	ds_read_b128 v[248:251], v191 offset:23552
	global_load_lds_dwordx4 v[4:5], off
	v_lshl_add_u64 v[4:5], s[28:29], 0, v[174:175]
	s_add_u32 s2, s28, 0x20100
	v_lshl_add_u64 v[6:7], v[4:5], 0, s[76:77]
	s_mov_b32 m0, s42
	s_addc_u32 s3, s29, 0
	global_load_lds_dwordx4 v[6:7], off
	s_mov_b32 m0, s44
	v_mov_b32_e32 v169, v219
	global_load_lds_dwordx4 v164, s[2:3]
	s_mov_b32 m0, s45
	v_lshl_add_u64 v[6:7], s[6:7], 0, v[168:169]
	global_load_lds_dwordx4 v174, s[2:3]
	v_lshl_add_u64 v[8:9], v[6:7], 0, s[76:77]
	s_mov_b32 m0, s46
	v_mov_b32_e32 v167, v219
	global_load_lds_dwordx4 v[8:9], off
	v_lshl_add_u64 v[8:9], s[6:7], 0, v[166:167]
	s_mov_b32 m0, s47
	v_lshl_add_u64 v[20:21], v[8:9], 0, s[76:77]
	global_load_lds_dwordx4 v[20:21], off
	s_waitcnt vmcnt(8)
	s_waitcnt lgkmcnt(0)
	s_barrier
	s_setprio 1
	v_mov_b64_e32 v[92:93], s[54:55]
	v_mov_b64_e32 v[84:85], s[54:55]
	v_mov_b64_e32 v[76:77], s[54:55]
	v_mov_b64_e32 v[68:69], s[54:55]
	v_mov_b64_e32 v[60:61], s[54:55]
	v_mov_b64_e32 v[50:51], s[52:53]
	v_mov_b64_e32 v[42:43], s[52:53]
	v_mov_b64_e32 v[38:39], s[52:53]
	v_mov_b64_e32 v[90:91], s[52:53]
	v_mov_b64_e32 v[82:83], s[52:53]
	v_mov_b64_e32 v[74:75], s[52:53]
	v_mov_b64_e32 v[66:67], s[52:53]
	v_mov_b64_e32 v[58:59], s[52:53]
	v_mov_b64_e32 v[52:53], s[54:55]
	v_mov_b64_e32 v[44:45], s[54:55]
	v_mov_b64_e32 v[40:41], s[54:55]
	s_waitcnt lgkmcnt(0)
	v_mfma_scale_f32_16x16x128_f8f6f4 v[90:93], v[10:17], v[200:207], v[90:93], v232, v232 op_sel_hi:[0,0,0]
	v_mfma_scale_f32_16x16x128_f8f6f4 v[82:85], v[24:31], v[200:207], v[82:85], v232, v232 op_sel_hi:[0,0,0]
	v_mfma_scale_f32_16x16x128_f8f6f4 v[74:77], v[10:17], v[208:215], v[74:77], v232, v232 op_sel_hi:[0,0,0]
	v_mfma_scale_f32_16x16x128_f8f6f4 v[66:69], v[24:31], v[208:215], v[66:69], v232, v232 op_sel_hi:[0,0,0]
	v_mfma_scale_f32_16x16x128_f8f6f4 v[58:61], v[10:17], v[222:229], v[58:61], v232, v232 op_sel_hi:[0,0,0]
	v_mfma_scale_f32_16x16x128_f8f6f4 v[50:53], v[24:31], v[222:229], v[50:53], v232, v232 op_sel_hi:[0,0,0]
	v_mfma_scale_f32_16x16x128_f8f6f4 v[42:45], v[10:17], v[244:251], v[42:45], v232, v232 op_sel_hi:[0,0,0]
	v_mfma_scale_f32_16x16x128_f8f6f4 v[38:41], v[24:31], v[244:251], v[38:41], v232, v232 op_sel_hi:[0,0,0]
	v_mov_b64_e32 v[96:97], s[54:55]
	v_mov_b64_e32 v[88:89], s[54:55]
	v_mov_b64_e32 v[80:81], s[54:55]
	v_mov_b64_e32 v[72:73], s[54:55]
	v_mov_b64_e32 v[64:65], s[54:55]
	v_mov_b64_e32 v[56:57], s[54:55]
	v_mov_b64_e32 v[46:47], s[52:53]
	v_mov_b64_e32 v[94:95], s[52:53]
	v_mov_b64_e32 v[86:87], s[52:53]
	v_mov_b64_e32 v[78:79], s[52:53]
	v_mov_b64_e32 v[70:71], s[52:53]
	v_mov_b64_e32 v[62:63], s[52:53]
	v_mov_b64_e32 v[54:55], s[52:53]
	v_mov_b64_e32 v[48:49], s[54:55]
	v_mfma_scale_f32_16x16x128_f8f6f4 v[94:97], v[182:189], v[200:207], v[94:97], v232, v232 op_sel_hi:[0,0,0]
	v_mfma_scale_f32_16x16x128_f8f6f4 v[86:89], v[192:199], v[200:207], v[86:89], v232, v232 op_sel_hi:[0,0,0]
	v_mfma_scale_f32_16x16x128_f8f6f4 v[78:81], v[182:189], v[208:215], v[78:81], v232, v232 op_sel_hi:[0,0,0]
	v_mfma_scale_f32_16x16x128_f8f6f4 v[70:73], v[192:199], v[208:215], v[70:73], v232, v232 op_sel_hi:[0,0,0]
	v_mfma_scale_f32_16x16x128_f8f6f4 v[62:65], v[182:189], v[222:229], v[62:65], v232, v232 op_sel_hi:[0,0,0]
	v_mfma_scale_f32_16x16x128_f8f6f4 v[54:57], v[192:199], v[222:229], v[54:57], v232, v232 op_sel_hi:[0,0,0]
	v_mfma_scale_f32_16x16x128_f8f6f4 v[46:49], v[182:189], v[244:251], v[46:49], v232, v232 op_sel_hi:[0,0,0]
	v_mfma_scale_f32_16x16x128_f8f6f4 v[34:37], v[192:199], v[244:251], v[34:37], v232, v232 op_sel_hi:[0,0,0]
	s_setprio 0
	s_barrier
	v_add_u32_e32 v192, s50, v190
	v_add_u32_e32 v193, s61, v190
	ds_read_b128 v[10:13], v192
	ds_read_b128 v[14:17], v192 offset:1024
	ds_read_b128 v[24:27], v192 offset:2048
	ds_read_b128 v[28:31], v192 offset:3072
	ds_read_b128 v[182:185], v193
	ds_read_b128 v[186:189], v193 offset:1024
	ds_read_b128 v[194:197], v193 offset:2048
	ds_read_b128 v[198:201], v193 offset:3072
	s_mov_b32 m0, s48
	v_lshl_add_u64 v[20:21], v[178:179], 0, s[76:77]
	ds_read_b128 v[202:205], v191 offset:32768
	ds_read_b128 v[206:209], v191 offset:33792
	ds_read_b128 v[210:213], v191 offset:34816
	ds_read_b128 v[214:217], v191 offset:35840
	ds_read_b128 v[222:225], v191 offset:36864
	ds_read_b128 v[226:229], v191 offset:37888
	ds_read_b128 v[244:247], v191 offset:38912
	ds_read_b128 v[248:251], v191 offset:39936
	global_load_lds_dwordx4 v[20:21], off
	s_mov_b32 m0, s49
	v_lshl_add_u64 v[20:21], v[180:181], 0, s[76:77]
	global_load_lds_dwordx4 v[20:21], off
	s_waitcnt vmcnt(8)
	s_waitcnt lgkmcnt(0)
	s_barrier
	s_setprio 1
	v_mfma_scale_f32_16x16x128_f8f6f4 v[154:157], v[10:17], v[202:209], v[154:157], v232, v232 op_sel_hi:[0,0,0]
	v_mfma_scale_f32_16x16x128_f8f6f4 v[146:149], v[24:31], v[202:209], v[146:149], v232, v232 op_sel_hi:[0,0,0]
	v_mfma_scale_f32_16x16x128_f8f6f4 v[138:141], v[10:17], v[210:217], v[138:141], v232, v232 op_sel_hi:[0,0,0]
	v_mfma_scale_f32_16x16x128_f8f6f4 v[130:133], v[24:31], v[210:217], v[130:133], v232, v232 op_sel_hi:[0,0,0]
	v_mfma_scale_f32_16x16x128_f8f6f4 v[122:125], v[10:17], v[222:229], v[122:125], v232, v232 op_sel_hi:[0,0,0]
	v_mfma_scale_f32_16x16x128_f8f6f4 v[114:117], v[24:31], v[222:229], v[114:117], v232, v232 op_sel_hi:[0,0,0]
	v_mfma_scale_f32_16x16x128_f8f6f4 v[106:109], v[10:17], v[244:251], v[106:109], v232, v232 op_sel_hi:[0,0,0]
	v_mfma_scale_f32_16x16x128_f8f6f4 v[98:101], v[24:31], v[244:251], v[98:101], v232, v232 op_sel_hi:[0,0,0]
	v_mfma_scale_f32_16x16x128_f8f6f4 v[158:161], v[182:189], v[202:209], v[158:161], v232, v232 op_sel_hi:[0,0,0]
	v_mfma_scale_f32_16x16x128_f8f6f4 v[150:153], v[194:201], v[202:209], v[150:153], v232, v232 op_sel_hi:[0,0,0]
	v_mfma_scale_f32_16x16x128_f8f6f4 v[142:145], v[182:189], v[210:217], v[142:145], v232, v232 op_sel_hi:[0,0,0]
	v_mfma_scale_f32_16x16x128_f8f6f4 v[134:137], v[194:201], v[210:217], v[134:137], v232, v232 op_sel_hi:[0,0,0]
	v_mfma_scale_f32_16x16x128_f8f6f4 v[126:129], v[182:189], v[222:229], v[126:129], v232, v232 op_sel_hi:[0,0,0]
	v_mfma_scale_f32_16x16x128_f8f6f4 v[118:121], v[194:201], v[222:229], v[118:121], v232, v232 op_sel_hi:[0,0,0]
	v_mfma_scale_f32_16x16x128_f8f6f4 v[110:113], v[182:189], v[244:251], v[110:113], v232, v232 op_sel_hi:[0,0,0]
	v_mfma_scale_f32_16x16x128_f8f6f4 v[102:105], v[194:201], v[244:251], v[102:105], v232, v232 op_sel_hi:[0,0,0]
	s_setprio 0
	s_barrier
	s_mov_b64 s[52:53], 0x180
	s_mov_b32 m0, s51
	v_lshl_add_u64 v[20:21], v[2:3], 0, s[52:53]
	ds_read_b128 v[202:205], v191 offset:49152
	ds_read_b128 v[206:209], v191 offset:50176
	ds_read_b128 v[210:213], v191 offset:51200
	ds_read_b128 v[214:217], v191 offset:52224
	ds_read_b128 v[222:225], v191 offset:53248
	ds_read_b128 v[226:229], v191 offset:54272
	ds_read_b128 v[244:247], v191 offset:55296
	ds_read_b128 v[248:251], v191 offset:56320
	global_load_lds_dwordx4 v[20:21], off
	v_lshl_add_u64 v[20:21], v[4:5], 0, s[52:53]
	s_mov_b32 m0, s56
	s_add_u32 s2, s28, 0x20180
	global_load_lds_dwordx4 v[20:21], off
	s_addc_u32 s3, s29, 0
	s_mov_b32 m0, s62
	v_lshl_add_u64 v[20:21], v[6:7], 0, s[52:53]
	global_load_lds_dwordx4 v164, s[2:3]
	s_mov_b32 m0, s63
	s_nop 0
	global_load_lds_dwordx4 v174, s[2:3]
	s_mov_b32 m0, s57
	s_nop 0
	global_load_lds_dwordx4 v[20:21], off
	s_mov_b32 m0, s60
	v_lshl_add_u64 v[20:21], v[8:9], 0, s[52:53]
	global_load_lds_dwordx4 v[20:21], off
	s_waitcnt vmcnt(8)
	s_waitcnt lgkmcnt(0)
	s_barrier
	s_setprio 1
	v_mfma_scale_f32_16x16x128_f8f6f4 v[90:93], v[10:17], v[202:209], v[90:93], v232, v232 op_sel_hi:[0,0,0]
	v_mfma_scale_f32_16x16x128_f8f6f4 v[82:85], v[24:31], v[202:209], v[82:85], v232, v232 op_sel_hi:[0,0,0]
	v_mfma_scale_f32_16x16x128_f8f6f4 v[74:77], v[10:17], v[210:217], v[74:77], v232, v232 op_sel_hi:[0,0,0]
	v_mfma_scale_f32_16x16x128_f8f6f4 v[66:69], v[24:31], v[210:217], v[66:69], v232, v232 op_sel_hi:[0,0,0]
	v_mfma_scale_f32_16x16x128_f8f6f4 v[58:61], v[10:17], v[222:229], v[58:61], v232, v232 op_sel_hi:[0,0,0]
	v_mfma_scale_f32_16x16x128_f8f6f4 v[50:53], v[24:31], v[222:229], v[50:53], v232, v232 op_sel_hi:[0,0,0]
	v_mfma_scale_f32_16x16x128_f8f6f4 v[42:45], v[10:17], v[244:251], v[42:45], v232, v232 op_sel_hi:[0,0,0]
	v_mfma_scale_f32_16x16x128_f8f6f4 v[38:41], v[24:31], v[244:251], v[38:41], v232, v232 op_sel_hi:[0,0,0]
	v_mfma_scale_f32_16x16x128_f8f6f4 v[94:97], v[182:189], v[202:209], v[94:97], v232, v232 op_sel_hi:[0,0,0]
	v_mfma_scale_f32_16x16x128_f8f6f4 v[86:89], v[194:201], v[202:209], v[86:89], v232, v232 op_sel_hi:[0,0,0]
	v_mfma_scale_f32_16x16x128_f8f6f4 v[78:81], v[182:189], v[210:217], v[78:81], v232, v232 op_sel_hi:[0,0,0]
	v_mfma_scale_f32_16x16x128_f8f6f4 v[70:73], v[194:201], v[210:217], v[70:73], v232, v232 op_sel_hi:[0,0,0]
	v_mfma_scale_f32_16x16x128_f8f6f4 v[62:65], v[182:189], v[222:229], v[62:65], v232, v232 op_sel_hi:[0,0,0]
	v_mfma_scale_f32_16x16x128_f8f6f4 v[54:57], v[194:201], v[222:229], v[54:57], v232, v232 op_sel_hi:[0,0,0]
	v_mfma_scale_f32_16x16x128_f8f6f4 v[46:49], v[182:189], v[244:251], v[46:49], v232, v232 op_sel_hi:[0,0,0]
	v_mfma_scale_f32_16x16x128_f8f6f4 v[34:37], v[194:201], v[244:251], v[34:37], v232, v232 op_sel_hi:[0,0,0]
	s_setprio 0
	s_barrier
	s_andn2_b64 vcc, exec, s[8:9]
	s_cbranch_vccnz .LBB0_1266
	s_and_b64 vcc, exec, s[4:5]
	s_mov_b64 s[2:3], 0
	s_cbranch_vccnz .LBB0_1267
	v_mov_b32_e32 v10, s88
	ds_read_b128 v[10:13], v10
	s_movk_i32 s70, 0xe00
	s_waitcnt lgkmcnt(0)
	v_readfirstlane_b32 s23, v10
	s_cmp_lt_i32 s23, 0
	v_readfirstlane_b32 s2, v12
	s_cbranch_scc1 .LBB0_1287
	s_ashr_i32 s90, s2, 16
	s_mov_b32 s22, s23
	s_branch .LBB0_1268

.LBB0_1269:
	ds_read_b128 v[10:13], v18
	ds_read_b128 v[14:17], v18 offset:1024
	ds_read_b128 v[24:27], v18 offset:2048
	ds_read_b128 v[28:31], v18 offset:3072
	ds_read_b128 v[182:185], v22
	ds_read_b128 v[186:189], v22 offset:1024
	ds_read_b128 v[194:197], v22 offset:2048
	ds_read_b128 v[198:201], v22 offset:3072
	s_mov_b64 s[2:3], 0x180
	s_mov_b32 m0, s31
	v_lshl_add_u64 v[20:21], v[178:179], 0, s[2:3]
	ds_read_b128 v[202:205], v191
	ds_read_b128 v[206:209], v191 offset:1024
	ds_read_b128 v[210:213], v191 offset:2048
	ds_read_b128 v[214:217], v191 offset:3072
	ds_read_b128 v[222:225], v191 offset:4096
	ds_read_b128 v[226:229], v191 offset:5120
	ds_read_b128 v[244:247], v191 offset:6144
	ds_read_b128 v[248:251], v191 offset:7168
	global_load_lds_dwordx4 v[20:21], off
	s_mov_b32 m0, s30
	v_lshl_add_u64 v[20:21], v[180:181], 0, s[2:3]
	global_load_lds_dwordx4 v[20:21], off
	s_waitcnt vmcnt(8)
	s_waitcnt lgkmcnt(0)
	s_barrier
	s_setprio 1
	v_mfma_scale_f32_16x16x128_f8f6f4 v[154:157], v[10:17], v[202:209], v[154:157], v232, v232 op_sel_hi:[0,0,0]
	v_mfma_scale_f32_16x16x128_f8f6f4 v[146:149], v[24:31], v[202:209], v[146:149], v232, v232 op_sel_hi:[0,0,0]
	v_mfma_scale_f32_16x16x128_f8f6f4 v[138:141], v[10:17], v[210:217], v[138:141], v232, v232 op_sel_hi:[0,0,0]
	v_mfma_scale_f32_16x16x128_f8f6f4 v[130:133], v[24:31], v[210:217], v[130:133], v232, v232 op_sel_hi:[0,0,0]
	v_mfma_scale_f32_16x16x128_f8f6f4 v[122:125], v[10:17], v[222:229], v[122:125], v232, v232 op_sel_hi:[0,0,0]
	v_mfma_scale_f32_16x16x128_f8f6f4 v[114:117], v[24:31], v[222:229], v[114:117], v232, v232 op_sel_hi:[0,0,0]
	v_mfma_scale_f32_16x16x128_f8f6f4 v[106:109], v[10:17], v[244:251], v[106:109], v232, v232 op_sel_hi:[0,0,0]
	v_mfma_scale_f32_16x16x128_f8f6f4 v[98:101], v[24:31], v[244:251], v[98:101], v232, v232 op_sel_hi:[0,0,0]
	v_mfma_scale_f32_16x16x128_f8f6f4 v[158:161], v[182:189], v[202:209], v[158:161], v232, v232 op_sel_hi:[0,0,0]
	v_mfma_scale_f32_16x16x128_f8f6f4 v[150:153], v[194:201], v[202:209], v[150:153], v232, v232 op_sel_hi:[0,0,0]
	v_mfma_scale_f32_16x16x128_f8f6f4 v[142:145], v[182:189], v[210:217], v[142:145], v232, v232 op_sel_hi:[0,0,0]
	v_mfma_scale_f32_16x16x128_f8f6f4 v[134:137], v[194:201], v[210:217], v[134:137], v232, v232 op_sel_hi:[0,0,0]
	v_mfma_scale_f32_16x16x128_f8f6f4 v[126:129], v[182:189], v[222:229], v[126:129], v232, v232 op_sel_hi:[0,0,0]
	v_mfma_scale_f32_16x16x128_f8f6f4 v[118:121], v[194:201], v[222:229], v[118:121], v232, v232 op_sel_hi:[0,0,0]
	v_mfma_scale_f32_16x16x128_f8f6f4 v[110:113], v[182:189], v[244:251], v[110:113], v232, v232 op_sel_hi:[0,0,0]
	v_mfma_scale_f32_16x16x128_f8f6f4 v[102:105], v[194:201], v[244:251], v[102:105], v232, v232 op_sel_hi:[0,0,0]
	s_setprio 0
	s_barrier
	s_mov_b32 m0, s41
	s_add_u32 s2, s28, 0x20200
	v_lshl_add_u64 v[20:21], v[2:3], 0, s[66:67]
	s_addc_u32 s3, s29, 0
	ds_read_b128 v[202:205], v191 offset:16384
	ds_read_b128 v[206:209], v191 offset:17408
	ds_read_b128 v[210:213], v191 offset:18432
	ds_read_b128 v[214:217], v191 offset:19456
	ds_read_b128 v[222:225], v191 offset:20480
	ds_read_b128 v[226:229], v191 offset:21504
	ds_read_b128 v[244:247], v191 offset:22528
	ds_read_b128 v[248:251], v191 offset:23552
	global_load_lds_dwordx4 v[20:21], off
	s_mov_b32 m0, s42
	v_lshl_add_u64 v[20:21], v[4:5], 0, s[66:67]
	global_load_lds_dwordx4 v[20:21], off
	s_mov_b32 m0, s44
	v_lshl_add_u64 v[20:21], s[2:3], 0, v[164:165]
	global_load_lds_dwordx4 v[20:21], off
	s_mov_b32 m0, s45
	v_lshl_add_u64 v[20:21], s[2:3], 0, v[174:175]
	global_load_lds_dwordx4 v[20:21], off
	s_mov_b32 m0, s46
	v_lshl_add_u64 v[20:21], v[6:7], 0, s[66:67]
	global_load_lds_dwordx4 v[20:21], off
	s_mov_b32 m0, s47
	v_lshl_add_u64 v[20:21], v[8:9], 0, s[66:67]
	global_load_lds_dwordx4 v[20:21], off
	s_waitcnt vmcnt(8)
	s_waitcnt lgkmcnt(0)
	s_barrier
	s_setprio 1
	v_mfma_scale_f32_16x16x128_f8f6f4 v[90:93], v[10:17], v[202:209], v[90:93], v232, v232 op_sel_hi:[0,0,0]
	v_mfma_scale_f32_16x16x128_f8f6f4 v[82:85], v[24:31], v[202:209], v[82:85], v232, v232 op_sel_hi:[0,0,0]
	v_mfma_scale_f32_16x16x128_f8f6f4 v[74:77], v[10:17], v[210:217], v[74:77], v232, v232 op_sel_hi:[0,0,0]
	v_mfma_scale_f32_16x16x128_f8f6f4 v[66:69], v[24:31], v[210:217], v[66:69], v232, v232 op_sel_hi:[0,0,0]
	v_mfma_scale_f32_16x16x128_f8f6f4 v[58:61], v[10:17], v[222:229], v[58:61], v232, v232 op_sel_hi:[0,0,0]
	v_mfma_scale_f32_16x16x128_f8f6f4 v[50:53], v[24:31], v[222:229], v[50:53], v232, v232 op_sel_hi:[0,0,0]
	v_mfma_scale_f32_16x16x128_f8f6f4 v[42:45], v[10:17], v[244:251], v[42:45], v232, v232 op_sel_hi:[0,0,0]
	v_mfma_scale_f32_16x16x128_f8f6f4 v[38:41], v[24:31], v[244:251], v[38:41], v232, v232 op_sel_hi:[0,0,0]
	v_mfma_scale_f32_16x16x128_f8f6f4 v[94:97], v[182:189], v[202:209], v[94:97], v232, v232 op_sel_hi:[0,0,0]
	v_mfma_scale_f32_16x16x128_f8f6f4 v[86:89], v[194:201], v[202:209], v[86:89], v232, v232 op_sel_hi:[0,0,0]
	v_mfma_scale_f32_16x16x128_f8f6f4 v[78:81], v[182:189], v[210:217], v[78:81], v232, v232 op_sel_hi:[0,0,0]
	v_mfma_scale_f32_16x16x128_f8f6f4 v[70:73], v[194:201], v[210:217], v[70:73], v232, v232 op_sel_hi:[0,0,0]
	v_mfma_scale_f32_16x16x128_f8f6f4 v[62:65], v[182:189], v[222:229], v[62:65], v232, v232 op_sel_hi:[0,0,0]
	v_mfma_scale_f32_16x16x128_f8f6f4 v[54:57], v[194:201], v[222:229], v[54:57], v232, v232 op_sel_hi:[0,0,0]
	v_mfma_scale_f32_16x16x128_f8f6f4 v[46:49], v[182:189], v[244:251], v[46:49], v232, v232 op_sel_hi:[0,0,0]
	v_mfma_scale_f32_16x16x128_f8f6f4 v[34:37], v[194:201], v[244:251], v[34:37], v232, v232 op_sel_hi:[0,0,0]
	s_setprio 0
	s_barrier
	ds_read_b128 v[10:13], v192
	ds_read_b128 v[14:17], v192 offset:1024
	ds_read_b128 v[24:27], v192 offset:2048
	ds_read_b128 v[28:31], v192 offset:3072
	ds_read_b128 v[182:185], v193
	ds_read_b128 v[186:189], v193 offset:1024
	ds_read_b128 v[194:197], v193 offset:2048
	ds_read_b128 v[198:201], v193 offset:3072
	s_mov_b32 m0, s48
	v_lshl_add_u64 v[20:21], v[178:179], 0, s[66:67]
	ds_read_b128 v[202:205], v191 offset:32768
	ds_read_b128 v[206:209], v191 offset:33792
	ds_read_b128 v[210:213], v191 offset:34816
	ds_read_b128 v[214:217], v191 offset:35840
	ds_read_b128 v[222:225], v191 offset:36864
	ds_read_b128 v[226:229], v191 offset:37888
	ds_read_b128 v[244:247], v191 offset:38912
	ds_read_b128 v[248:251], v191 offset:39936
	global_load_lds_dwordx4 v[20:21], off
	s_mov_b32 m0, s49
	v_lshl_add_u64 v[20:21], v[180:181], 0, s[66:67]
	global_load_lds_dwordx4 v[20:21], off
	s_waitcnt vmcnt(8)
	s_waitcnt lgkmcnt(0)
	s_barrier
	s_setprio 1
	v_mfma_scale_f32_16x16x128_f8f6f4 v[154:157], v[10:17], v[202:209], v[154:157], v232, v232 op_sel_hi:[0,0,0]
	v_mfma_scale_f32_16x16x128_f8f6f4 v[146:149], v[24:31], v[202:209], v[146:149], v232, v232 op_sel_hi:[0,0,0]
	v_mfma_scale_f32_16x16x128_f8f6f4 v[138:141], v[10:17], v[210:217], v[138:141], v232, v232 op_sel_hi:[0,0,0]
	v_mfma_scale_f32_16x16x128_f8f6f4 v[130:133], v[24:31], v[210:217], v[130:133], v232, v232 op_sel_hi:[0,0,0]
	v_mfma_scale_f32_16x16x128_f8f6f4 v[122:125], v[10:17], v[222:229], v[122:125], v232, v232 op_sel_hi:[0,0,0]
	v_mfma_scale_f32_16x16x128_f8f6f4 v[114:117], v[24:31], v[222:229], v[114:117], v232, v232 op_sel_hi:[0,0,0]
	v_mfma_scale_f32_16x16x128_f8f6f4 v[106:109], v[10:17], v[244:251], v[106:109], v232, v232 op_sel_hi:[0,0,0]
	v_mfma_scale_f32_16x16x128_f8f6f4 v[98:101], v[24:31], v[244:251], v[98:101], v232, v232 op_sel_hi:[0,0,0]
	v_mfma_scale_f32_16x16x128_f8f6f4 v[158:161], v[182:189], v[202:209], v[158:161], v232, v232 op_sel_hi:[0,0,0]
	v_mfma_scale_f32_16x16x128_f8f6f4 v[150:153], v[194:201], v[202:209], v[150:153], v232, v232 op_sel_hi:[0,0,0]
	v_mfma_scale_f32_16x16x128_f8f6f4 v[142:145], v[182:189], v[210:217], v[142:145], v232, v232 op_sel_hi:[0,0,0]
	v_mfma_scale_f32_16x16x128_f8f6f4 v[134:137], v[194:201], v[210:217], v[134:137], v232, v232 op_sel_hi:[0,0,0]
	v_mfma_scale_f32_16x16x128_f8f6f4 v[126:129], v[182:189], v[222:229], v[126:129], v232, v232 op_sel_hi:[0,0,0]
	v_mfma_scale_f32_16x16x128_f8f6f4 v[118:121], v[194:201], v[222:229], v[118:121], v232, v232 op_sel_hi:[0,0,0]
	v_mfma_scale_f32_16x16x128_f8f6f4 v[110:113], v[182:189], v[244:251], v[110:113], v232, v232 op_sel_hi:[0,0,0]
	v_mfma_scale_f32_16x16x128_f8f6f4 v[102:105], v[194:201], v[244:251], v[102:105], v232, v232 op_sel_hi:[0,0,0]
	s_setprio 0
	s_barrier
	s_mov_b64 s[52:53], 0x280
	s_mov_b32 m0, s51
	v_lshl_add_u64 v[20:21], v[2:3], 0, s[52:53]
	s_add_u32 s2, s28, 0x20280
	ds_read_b128 v[202:205], v191 offset:49152
	ds_read_b128 v[206:209], v191 offset:50176
	ds_read_b128 v[210:213], v191 offset:51200
	ds_read_b128 v[214:217], v191 offset:52224
	ds_read_b128 v[222:225], v191 offset:53248
	ds_read_b128 v[226:229], v191 offset:54272
	ds_read_b128 v[244:247], v191 offset:55296
	ds_read_b128 v[248:251], v191 offset:56320
	global_load_lds_dwordx4 v[20:21], off
	v_lshl_add_u64 v[20:21], v[4:5], 0, s[52:53]
	s_mov_b32 m0, s56
	s_addc_u32 s3, s29, 0
	global_load_lds_dwordx4 v[20:21], off
	s_mov_b32 m0, s62
	v_lshl_add_u64 v[20:21], s[2:3], 0, v[164:165]
	global_load_lds_dwordx4 v[20:21], off
	s_mov_b32 m0, s63
	v_lshl_add_u64 v[20:21], s[2:3], 0, v[174:175]
	global_load_lds_dwordx4 v[20:21], off
	s_mov_b32 m0, s57
	v_lshl_add_u64 v[20:21], v[6:7], 0, s[52:53]
	global_load_lds_dwordx4 v[20:21], off
	s_mov_b32 m0, s60
	v_lshl_add_u64 v[20:21], v[8:9], 0, s[52:53]
	global_load_lds_dwordx4 v[20:21], off
	s_waitcnt vmcnt(8)
	s_waitcnt lgkmcnt(0)
	s_barrier
	s_setprio 1
	v_mfma_scale_f32_16x16x128_f8f6f4 v[90:93], v[10:17], v[202:209], v[90:93], v232, v232 op_sel_hi:[0,0,0]
	v_mfma_scale_f32_16x16x128_f8f6f4 v[82:85], v[24:31], v[202:209], v[82:85], v232, v232 op_sel_hi:[0,0,0]
	v_mfma_scale_f32_16x16x128_f8f6f4 v[74:77], v[10:17], v[210:217], v[74:77], v232, v232 op_sel_hi:[0,0,0]
	v_mfma_scale_f32_16x16x128_f8f6f4 v[66:69], v[24:31], v[210:217], v[66:69], v232, v232 op_sel_hi:[0,0,0]
	v_mfma_scale_f32_16x16x128_f8f6f4 v[58:61], v[10:17], v[222:229], v[58:61], v232, v232 op_sel_hi:[0,0,0]
	v_mfma_scale_f32_16x16x128_f8f6f4 v[50:53], v[24:31], v[222:229], v[50:53], v232, v232 op_sel_hi:[0,0,0]
	v_mfma_scale_f32_16x16x128_f8f6f4 v[42:45], v[10:17], v[244:251], v[42:45], v232, v232 op_sel_hi:[0,0,0]
	v_mfma_scale_f32_16x16x128_f8f6f4 v[38:41], v[24:31], v[244:251], v[38:41], v232, v232 op_sel_hi:[0,0,0]
	v_mfma_scale_f32_16x16x128_f8f6f4 v[94:97], v[182:189], v[202:209], v[94:97], v232, v232 op_sel_hi:[0,0,0]
	v_mfma_scale_f32_16x16x128_f8f6f4 v[86:89], v[194:201], v[202:209], v[86:89], v232, v232 op_sel_hi:[0,0,0]
	v_mfma_scale_f32_16x16x128_f8f6f4 v[78:81], v[182:189], v[210:217], v[78:81], v232, v232 op_sel_hi:[0,0,0]
	v_mfma_scale_f32_16x16x128_f8f6f4 v[70:73], v[194:201], v[210:217], v[70:73], v232, v232 op_sel_hi:[0,0,0]
	v_mfma_scale_f32_16x16x128_f8f6f4 v[62:65], v[182:189], v[222:229], v[62:65], v232, v232 op_sel_hi:[0,0,0]
	v_mfma_scale_f32_16x16x128_f8f6f4 v[54:57], v[194:201], v[222:229], v[54:57], v232, v232 op_sel_hi:[0,0,0]
	v_mfma_scale_f32_16x16x128_f8f6f4 v[46:49], v[182:189], v[244:251], v[46:49], v232, v232 op_sel_hi:[0,0,0]
	v_mfma_scale_f32_16x16x128_f8f6f4 v[34:37], v[194:201], v[244:251], v[34:37], v232, v232 op_sel_hi:[0,0,0]
	s_setprio 0
	s_barrier
	ds_read_b128 v[10:13], v18
	ds_read_b128 v[14:17], v18 offset:1024
	ds_read_b128 v[24:27], v18 offset:2048
	ds_read_b128 v[28:31], v18 offset:3072
	ds_read_b128 v[182:185], v22
	ds_read_b128 v[186:189], v22 offset:1024
	ds_read_b128 v[194:197], v22 offset:2048
	ds_read_b128 v[198:201], v22 offset:3072
	s_mov_b32 m0, s31
	v_lshl_add_u64 v[20:21], v[178:179], 0, s[52:53]
	ds_read_b128 v[202:205], v191
	ds_read_b128 v[206:209], v191 offset:1024
	ds_read_b128 v[210:213], v191 offset:2048
	ds_read_b128 v[214:217], v191 offset:3072
	ds_read_b128 v[222:225], v191 offset:4096
	ds_read_b128 v[226:229], v191 offset:5120
	ds_read_b128 v[244:247], v191 offset:6144
	ds_read_b128 v[248:251], v191 offset:7168
	global_load_lds_dwordx4 v[20:21], off
	s_mov_b32 m0, s30
	v_lshl_add_u64 v[20:21], v[180:181], 0, s[52:53]
	global_load_lds_dwordx4 v[20:21], off
	s_waitcnt vmcnt(8)
	s_waitcnt lgkmcnt(0)
	s_barrier
	s_setprio 1
	v_mfma_scale_f32_16x16x128_f8f6f4 v[154:157], v[10:17], v[202:209], v[154:157], v232, v232 op_sel_hi:[0,0,0]
	v_mfma_scale_f32_16x16x128_f8f6f4 v[146:149], v[24:31], v[202:209], v[146:149], v232, v232 op_sel_hi:[0,0,0]
	v_mfma_scale_f32_16x16x128_f8f6f4 v[138:141], v[10:17], v[210:217], v[138:141], v232, v232 op_sel_hi:[0,0,0]
	v_mfma_scale_f32_16x16x128_f8f6f4 v[130:133], v[24:31], v[210:217], v[130:133], v232, v232 op_sel_hi:[0,0,0]
	v_mfma_scale_f32_16x16x128_f8f6f4 v[122:125], v[10:17], v[222:229], v[122:125], v232, v232 op_sel_hi:[0,0,0]
	v_mfma_scale_f32_16x16x128_f8f6f4 v[114:117], v[24:31], v[222:229], v[114:117], v232, v232 op_sel_hi:[0,0,0]
	v_mfma_scale_f32_16x16x128_f8f6f4 v[106:109], v[10:17], v[244:251], v[106:109], v232, v232 op_sel_hi:[0,0,0]
	v_mfma_scale_f32_16x16x128_f8f6f4 v[98:101], v[24:31], v[244:251], v[98:101], v232, v232 op_sel_hi:[0,0,0]
	v_mfma_scale_f32_16x16x128_f8f6f4 v[158:161], v[182:189], v[202:209], v[158:161], v232, v232 op_sel_hi:[0,0,0]
	v_mfma_scale_f32_16x16x128_f8f6f4 v[150:153], v[194:201], v[202:209], v[150:153], v232, v232 op_sel_hi:[0,0,0]
	v_mfma_scale_f32_16x16x128_f8f6f4 v[142:145], v[182:189], v[210:217], v[142:145], v232, v232 op_sel_hi:[0,0,0]
	v_mfma_scale_f32_16x16x128_f8f6f4 v[134:137], v[194:201], v[210:217], v[134:137], v232, v232 op_sel_hi:[0,0,0]
	v_mfma_scale_f32_16x16x128_f8f6f4 v[126:129], v[182:189], v[222:229], v[126:129], v232, v232 op_sel_hi:[0,0,0]
	v_mfma_scale_f32_16x16x128_f8f6f4 v[118:121], v[194:201], v[222:229], v[118:121], v232, v232 op_sel_hi:[0,0,0]
	v_mfma_scale_f32_16x16x128_f8f6f4 v[110:113], v[182:189], v[244:251], v[110:113], v232, v232 op_sel_hi:[0,0,0]
	v_mfma_scale_f32_16x16x128_f8f6f4 v[102:105], v[194:201], v[244:251], v[102:105], v232, v232 op_sel_hi:[0,0,0]
	s_setprio 0
	s_barrier
	s_mov_b64 s[52:53], 0x300
	s_mov_b32 m0, s41
	s_add_u32 s2, s28, 0x20300
	v_lshl_add_u64 v[20:21], v[2:3], 0, s[52:53]
	s_addc_u32 s3, s29, 0
	ds_read_b128 v[202:205], v191 offset:16384
	ds_read_b128 v[206:209], v191 offset:17408
	ds_read_b128 v[210:213], v191 offset:18432
	ds_read_b128 v[214:217], v191 offset:19456
	ds_read_b128 v[222:225], v191 offset:20480
	ds_read_b128 v[226:229], v191 offset:21504
	ds_read_b128 v[244:247], v191 offset:22528
	ds_read_b128 v[248:251], v191 offset:23552
	global_load_lds_dwordx4 v[20:21], off
	v_lshl_add_u64 v[20:21], v[4:5], 0, s[52:53]
	s_mov_b32 m0, s42
	v_lshl_add_u64 v[32:33], s[2:3], 0, v[174:175]
	global_load_lds_dwordx4 v[20:21], off
	v_lshl_add_u64 v[20:21], s[2:3], 0, v[164:165]
	s_mov_b32 m0, s44
	v_lshl_add_u64 v[234:235], v[6:7], 0, s[52:53]
	global_load_lds_dwordx4 v[20:21], off
	s_mov_b32 m0, s45
	s_nop 0
	global_load_lds_dwordx4 v[32:33], off
	s_mov_b32 m0, s46
	s_nop 0
	global_load_lds_dwordx4 v[234:235], off
	s_mov_b32 m0, s47
	v_lshl_add_u64 v[234:235], v[8:9], 0, s[52:53]
	global_load_lds_dwordx4 v[234:235], off
	s_waitcnt vmcnt(8)
	s_waitcnt lgkmcnt(0)
	s_barrier
	s_setprio 1
	v_mfma_scale_f32_16x16x128_f8f6f4 v[90:93], v[10:17], v[202:209], v[90:93], v232, v232 op_sel_hi:[0,0,0]
	v_mfma_scale_f32_16x16x128_f8f6f4 v[82:85], v[24:31], v[202:209], v[82:85], v232, v232 op_sel_hi:[0,0,0]
	v_mfma_scale_f32_16x16x128_f8f6f4 v[74:77], v[10:17], v[210:217], v[74:77], v232, v232 op_sel_hi:[0,0,0]
	v_mfma_scale_f32_16x16x128_f8f6f4 v[66:69], v[24:31], v[210:217], v[66:69], v232, v232 op_sel_hi:[0,0,0]
	v_mfma_scale_f32_16x16x128_f8f6f4 v[58:61], v[10:17], v[222:229], v[58:61], v232, v232 op_sel_hi:[0,0,0]
	v_mfma_scale_f32_16x16x128_f8f6f4 v[50:53], v[24:31], v[222:229], v[50:53], v232, v232 op_sel_hi:[0,0,0]
	v_mfma_scale_f32_16x16x128_f8f6f4 v[42:45], v[10:17], v[244:251], v[42:45], v232, v232 op_sel_hi:[0,0,0]
	v_mfma_scale_f32_16x16x128_f8f6f4 v[38:41], v[24:31], v[244:251], v[38:41], v232, v232 op_sel_hi:[0,0,0]
	v_mfma_scale_f32_16x16x128_f8f6f4 v[94:97], v[182:189], v[202:209], v[94:97], v232, v232 op_sel_hi:[0,0,0]
	v_mfma_scale_f32_16x16x128_f8f6f4 v[86:89], v[194:201], v[202:209], v[86:89], v232, v232 op_sel_hi:[0,0,0]
	v_mfma_scale_f32_16x16x128_f8f6f4 v[78:81], v[182:189], v[210:217], v[78:81], v232, v232 op_sel_hi:[0,0,0]
	v_mfma_scale_f32_16x16x128_f8f6f4 v[70:73], v[194:201], v[210:217], v[70:73], v232, v232 op_sel_hi:[0,0,0]
	v_mfma_scale_f32_16x16x128_f8f6f4 v[62:65], v[182:189], v[222:229], v[62:65], v232, v232 op_sel_hi:[0,0,0]
	v_mfma_scale_f32_16x16x128_f8f6f4 v[54:57], v[194:201], v[222:229], v[54:57], v232, v232 op_sel_hi:[0,0,0]
	v_mfma_scale_f32_16x16x128_f8f6f4 v[46:49], v[182:189], v[244:251], v[46:49], v232, v232 op_sel_hi:[0,0,0]
	v_mfma_scale_f32_16x16x128_f8f6f4 v[34:37], v[194:201], v[244:251], v[34:37], v232, v232 op_sel_hi:[0,0,0]
	s_setprio 0
	s_barrier
	ds_read_b128 v[10:13], v192
	ds_read_b128 v[14:17], v192 offset:1024
	ds_read_b128 v[24:27], v192 offset:2048
	ds_read_b128 v[28:31], v192 offset:3072
	ds_read_b128 v[182:185], v193
	ds_read_b128 v[186:189], v193 offset:1024
	ds_read_b128 v[194:197], v193 offset:2048
	ds_read_b128 v[198:201], v193 offset:3072
	s_mov_b32 m0, s48
	v_lshl_add_u64 v[234:235], v[178:179], 0, s[52:53]
	ds_read_b128 v[202:205], v191 offset:32768
	ds_read_b128 v[206:209], v191 offset:33792
	ds_read_b128 v[210:213], v191 offset:34816
	ds_read_b128 v[214:217], v191 offset:35840
	ds_read_b128 v[222:225], v191 offset:36864
	ds_read_b128 v[226:229], v191 offset:37888
	ds_read_b128 v[244:247], v191 offset:38912
	ds_read_b128 v[248:251], v191 offset:39936
	global_load_lds_dwordx4 v[234:235], off
	s_mov_b32 m0, s49
	v_lshl_add_u64 v[234:235], v[180:181], 0, s[52:53]
	global_load_lds_dwordx4 v[234:235], off
	s_waitcnt vmcnt(8)
	s_waitcnt lgkmcnt(0)
	s_barrier
	s_setprio 1
	v_mfma_scale_f32_16x16x128_f8f6f4 v[154:157], v[10:17], v[202:209], v[154:157], v232, v232 op_sel_hi:[0,0,0]
	v_mfma_scale_f32_16x16x128_f8f6f4 v[146:149], v[24:31], v[202:209], v[146:149], v232, v232 op_sel_hi:[0,0,0]
	v_mfma_scale_f32_16x16x128_f8f6f4 v[138:141], v[10:17], v[210:217], v[138:141], v232, v232 op_sel_hi:[0,0,0]
	v_mfma_scale_f32_16x16x128_f8f6f4 v[130:133], v[24:31], v[210:217], v[130:133], v232, v232 op_sel_hi:[0,0,0]
	v_mfma_scale_f32_16x16x128_f8f6f4 v[122:125], v[10:17], v[222:229], v[122:125], v232, v232 op_sel_hi:[0,0,0]
	v_mfma_scale_f32_16x16x128_f8f6f4 v[114:117], v[24:31], v[222:229], v[114:117], v232, v232 op_sel_hi:[0,0,0]
	v_mfma_scale_f32_16x16x128_f8f6f4 v[106:109], v[10:17], v[244:251], v[106:109], v232, v232 op_sel_hi:[0,0,0]
	v_mfma_scale_f32_16x16x128_f8f6f4 v[98:101], v[24:31], v[244:251], v[98:101], v232, v232 op_sel_hi:[0,0,0]
	v_mfma_scale_f32_16x16x128_f8f6f4 v[158:161], v[182:189], v[202:209], v[158:161], v232, v232 op_sel_hi:[0,0,0]
	v_mfma_scale_f32_16x16x128_f8f6f4 v[150:153], v[194:201], v[202:209], v[150:153], v232, v232 op_sel_hi:[0,0,0]
	v_mfma_scale_f32_16x16x128_f8f6f4 v[142:145], v[182:189], v[210:217], v[142:145], v232, v232 op_sel_hi:[0,0,0]
	v_mfma_scale_f32_16x16x128_f8f6f4 v[134:137], v[194:201], v[210:217], v[134:137], v232, v232 op_sel_hi:[0,0,0]
	v_mfma_scale_f32_16x16x128_f8f6f4 v[126:129], v[182:189], v[222:229], v[126:129], v232, v232 op_sel_hi:[0,0,0]
	v_mfma_scale_f32_16x16x128_f8f6f4 v[118:121], v[194:201], v[222:229], v[118:121], v232, v232 op_sel_hi:[0,0,0]
	v_mfma_scale_f32_16x16x128_f8f6f4 v[110:113], v[182:189], v[244:251], v[110:113], v232, v232 op_sel_hi:[0,0,0]
	v_mfma_scale_f32_16x16x128_f8f6f4 v[102:105], v[194:201], v[244:251], v[102:105], v232, v232 op_sel_hi:[0,0,0]
	s_setprio 0
	s_barrier
	s_mov_b64 s[2:3], 0x380
	s_mov_b32 m0, s51
	v_lshl_add_u64 v[2:3], v[2:3], 0, s[2:3]
	ds_read_b128 v[202:205], v191 offset:49152
	ds_read_b128 v[206:209], v191 offset:50176
	ds_read_b128 v[210:213], v191 offset:51200
	ds_read_b128 v[214:217], v191 offset:52224
	ds_read_b128 v[222:225], v191 offset:53248
	ds_read_b128 v[226:229], v191 offset:54272
	ds_read_b128 v[244:247], v191 offset:55296
	ds_read_b128 v[248:251], v191 offset:56320
	global_load_lds_dwordx4 v[2:3], off
	s_mov_b32 m0, s56
	v_lshl_add_u64 v[2:3], v[4:5], 0, s[2:3]
	global_load_lds_dwordx4 v[2:3], off
	s_mov_b32 m0, s62
	v_lshl_add_u64 v[2:3], v[20:21], 0, s[72:73]
	global_load_lds_dwordx4 v[2:3], off
	s_mov_b32 m0, s63
	v_lshl_add_u64 v[2:3], v[32:33], 0, s[72:73]
	global_load_lds_dwordx4 v[2:3], off
	s_mov_b32 m0, s57
	v_lshl_add_u64 v[2:3], v[6:7], 0, s[2:3]
	global_load_lds_dwordx4 v[2:3], off
	s_mov_b32 m0, s60
	v_lshl_add_u64 v[2:3], v[8:9], 0, s[2:3]
	global_load_lds_dwordx4 v[2:3], off
	s_waitcnt vmcnt(8)
	s_waitcnt lgkmcnt(0)
	s_barrier
	s_setprio 1
	v_mfma_scale_f32_16x16x128_f8f6f4 v[90:93], v[10:17], v[202:209], v[90:93], v232, v232 op_sel_hi:[0,0,0]
	v_mfma_scale_f32_16x16x128_f8f6f4 v[82:85], v[24:31], v[202:209], v[82:85], v232, v232 op_sel_hi:[0,0,0]
	v_mfma_scale_f32_16x16x128_f8f6f4 v[74:77], v[10:17], v[210:217], v[74:77], v232, v232 op_sel_hi:[0,0,0]
	v_mfma_scale_f32_16x16x128_f8f6f4 v[66:69], v[24:31], v[210:217], v[66:69], v232, v232 op_sel_hi:[0,0,0]
	v_mfma_scale_f32_16x16x128_f8f6f4 v[58:61], v[10:17], v[222:229], v[58:61], v232, v232 op_sel_hi:[0,0,0]
	v_mfma_scale_f32_16x16x128_f8f6f4 v[50:53], v[24:31], v[222:229], v[50:53], v232, v232 op_sel_hi:[0,0,0]
	v_mfma_scale_f32_16x16x128_f8f6f4 v[42:45], v[10:17], v[244:251], v[42:45], v232, v232 op_sel_hi:[0,0,0]
	v_mfma_scale_f32_16x16x128_f8f6f4 v[38:41], v[24:31], v[244:251], v[38:41], v232, v232 op_sel_hi:[0,0,0]
	v_mfma_scale_f32_16x16x128_f8f6f4 v[94:97], v[182:189], v[202:209], v[94:97], v232, v232 op_sel_hi:[0,0,0]
	v_mfma_scale_f32_16x16x128_f8f6f4 v[86:89], v[194:201], v[202:209], v[86:89], v232, v232 op_sel_hi:[0,0,0]
	v_mfma_scale_f32_16x16x128_f8f6f4 v[78:81], v[182:189], v[210:217], v[78:81], v232, v232 op_sel_hi:[0,0,0]
	v_mfma_scale_f32_16x16x128_f8f6f4 v[70:73], v[194:201], v[210:217], v[70:73], v232, v232 op_sel_hi:[0,0,0]
	v_mfma_scale_f32_16x16x128_f8f6f4 v[62:65], v[182:189], v[222:229], v[62:65], v232, v232 op_sel_hi:[0,0,0]
	v_mfma_scale_f32_16x16x128_f8f6f4 v[54:57], v[194:201], v[222:229], v[54:57], v232, v232 op_sel_hi:[0,0,0]
	v_mfma_scale_f32_16x16x128_f8f6f4 v[46:49], v[182:189], v[244:251], v[46:49], v232, v232 op_sel_hi:[0,0,0]
	v_mfma_scale_f32_16x16x128_f8f6f4 v[34:37], v[194:201], v[244:251], v[34:37], v232, v232 op_sel_hi:[0,0,0]
	s_setprio 0
	s_barrier
	ds_read_b128 v[10:13], v18
	ds_read_b128 v[14:17], v18 offset:1024
	ds_read_b128 v[26:29], v18 offset:2048
	ds_read_b128 v[30:33], v18 offset:3072
	ds_read_b128 v[2:5], v22
	ds_read_b128 v[6:9], v22 offset:1024
	ds_read_b128 v[18:21], v22 offset:2048
	ds_read_b128 v[22:25], v22 offset:3072
	s_mov_b32 m0, s31
	v_lshl_add_u64 v[178:179], v[178:179], 0, s[2:3]
	ds_read_b128 v[182:185], v191
	ds_read_b128 v[186:189], v191 offset:1024
	ds_read_b128 v[194:197], v191 offset:2048
	ds_read_b128 v[198:201], v191 offset:3072
	ds_read_b128 v[202:205], v191 offset:4096
	ds_read_b128 v[206:209], v191 offset:5120
	ds_read_b128 v[210:213], v191 offset:6144
	ds_read_b128 v[214:217], v191 offset:7168
	global_load_lds_dwordx4 v[178:179], off
	s_mov_b32 m0, s30
	v_lshl_add_u64 v[178:179], v[180:181], 0, s[2:3]
	global_load_lds_dwordx4 v[178:179], off
	s_waitcnt vmcnt(8)
	s_waitcnt lgkmcnt(0)
	s_barrier
	s_setprio 1
	v_mfma_scale_f32_16x16x128_f8f6f4 v[154:157], v[10:17], v[182:189], v[154:157], v232, v232 op_sel_hi:[0,0,0]
	v_mfma_scale_f32_16x16x128_f8f6f4 v[146:149], v[26:33], v[182:189], v[146:149], v232, v232 op_sel_hi:[0,0,0]
	v_mfma_scale_f32_16x16x128_f8f6f4 v[138:141], v[10:17], v[194:201], v[138:141], v232, v232 op_sel_hi:[0,0,0]
	v_mfma_scale_f32_16x16x128_f8f6f4 v[130:133], v[26:33], v[194:201], v[130:133], v232, v232 op_sel_hi:[0,0,0]
	v_mfma_scale_f32_16x16x128_f8f6f4 v[122:125], v[10:17], v[202:209], v[122:125], v232, v232 op_sel_hi:[0,0,0]
	v_mfma_scale_f32_16x16x128_f8f6f4 v[114:117], v[26:33], v[202:209], v[114:117], v232, v232 op_sel_hi:[0,0,0]
	v_mfma_scale_f32_16x16x128_f8f6f4 v[106:109], v[10:17], v[210:217], v[106:109], v232, v232 op_sel_hi:[0,0,0]
	v_mfma_scale_f32_16x16x128_f8f6f4 v[98:101], v[26:33], v[210:217], v[98:101], v232, v232 op_sel_hi:[0,0,0]
	v_mfma_scale_f32_16x16x128_f8f6f4 v[158:161], v[2:9], v[182:189], v[158:161], v232, v232 op_sel_hi:[0,0,0]
	v_mfma_scale_f32_16x16x128_f8f6f4 v[150:153], v[18:25], v[182:189], v[150:153], v232, v232 op_sel_hi:[0,0,0]
	v_mfma_scale_f32_16x16x128_f8f6f4 v[142:145], v[2:9], v[194:201], v[142:145], v232, v232 op_sel_hi:[0,0,0]
	v_mfma_scale_f32_16x16x128_f8f6f4 v[134:137], v[18:25], v[194:201], v[134:137], v232, v232 op_sel_hi:[0,0,0]
	v_mfma_scale_f32_16x16x128_f8f6f4 v[126:129], v[2:9], v[202:209], v[126:129], v232, v232 op_sel_hi:[0,0,0]
	v_mfma_scale_f32_16x16x128_f8f6f4 v[118:121], v[18:25], v[202:209], v[118:121], v232, v232 op_sel_hi:[0,0,0]
	v_mfma_scale_f32_16x16x128_f8f6f4 v[110:113], v[2:9], v[210:217], v[110:113], v232, v232 op_sel_hi:[0,0,0]
	v_mfma_scale_f32_16x16x128_f8f6f4 v[102:105], v[18:25], v[210:217], v[102:105], v232, v232 op_sel_hi:[0,0,0]
	s_setprio 0
	s_barrier
	s_and_b64 vcc, exec, s[4:5]
	s_mov_b64 s[2:3], 0
	s_cbranch_vccnz .LBB0_1272
	v_mov_b32_e32 v177, s88
	ds_read_b128 v[178:181], v177
	s_waitcnt lgkmcnt(0)
	v_readfirstlane_b32 s58, v178
	v_readfirstlane_b32 s4, v179
	s_cmp_lt_i32 s58, 0
	v_readfirstlane_b32 s5, v180
	s_cbranch_scc1 .LBB0_1272
	s_ashr_i32 s20, s5, 16
	s_and_b32 s91, s5, 0xffff
	s_lshl_b64 s[24:25], s[58:59], 21
	s_add_u32 s5, s34, s24
	s_addc_u32 s23, s35, s25
	s_ashr_i32 s21, s20, 31
	s_lshl_b64 s[24:25], s[20:21], 18
	s_add_u32 s24, s5, s24
	s_addc_u32 s25, s23, s25
	s_lshl_b32 s21, s4, 8
	s_add_u32 s4, s28, 0x20000
	s_addc_u32 s5, s29, 0
	s_branch .LBB0_1273

.LBB0_1282:
	s_mov_b32 m0, s41
	v_lshl_add_u64 v[178:179], s[28:29], 0, v[164:165]
	ds_read_b128 v[194:197], v191 offset:16384
	ds_read_b128 v[198:201], v191 offset:17408
	ds_read_b128 v[202:205], v191 offset:18432
	ds_read_b128 v[206:209], v191 offset:19456
	ds_read_b128 v[210:213], v191 offset:20480
	ds_read_b128 v[214:217], v191 offset:21504
	ds_read_b128 v[222:225], v191 offset:22528
	ds_read_b128 v[226:229], v191 offset:23552
	global_load_lds_dwordx4 v[178:179], off
	v_lshl_add_u64 v[180:181], s[28:29], 0, v[174:175]
	s_mov_b32 m0, s42
	v_lshl_add_u64 v[182:183], s[4:5], 0, v[164:165]
	global_load_lds_dwordx4 v[180:181], off
	s_mov_b32 m0, s44
	v_lshl_add_u64 v[184:185], s[4:5], 0, v[174:175]
	global_load_lds_dwordx4 v[182:183], off
	s_mov_b32 m0, s45
	v_lshl_add_u64 v[186:187], s[6:7], 0, v[168:169]
	global_load_lds_dwordx4 v[184:185], off
	s_mov_b32 m0, s46
	v_lshl_add_u64 v[188:189], s[6:7], 0, v[166:167]
	global_load_lds_dwordx4 v[186:187], off
	s_mov_b32 m0, s47
	s_nop 0
	global_load_lds_dwordx4 v[188:189], off
	s_waitcnt vmcnt(8)
	s_waitcnt lgkmcnt(0)
	s_barrier
	s_setprio 1
	v_mfma_scale_f32_16x16x128_f8f6f4 v[90:93], v[10:17], v[194:201], v[90:93], v232, v232 op_sel_hi:[0,0,0]
	v_mfma_scale_f32_16x16x128_f8f6f4 v[82:85], v[26:33], v[194:201], v[82:85], v232, v232 op_sel_hi:[0,0,0]
	v_mfma_scale_f32_16x16x128_f8f6f4 v[74:77], v[10:17], v[202:209], v[74:77], v232, v232 op_sel_hi:[0,0,0]
	v_mfma_scale_f32_16x16x128_f8f6f4 v[66:69], v[26:33], v[202:209], v[66:69], v232, v232 op_sel_hi:[0,0,0]
	v_mfma_scale_f32_16x16x128_f8f6f4 v[58:61], v[10:17], v[210:217], v[58:61], v232, v232 op_sel_hi:[0,0,0]
	v_mfma_scale_f32_16x16x128_f8f6f4 v[50:53], v[26:33], v[210:217], v[50:53], v232, v232 op_sel_hi:[0,0,0]
	v_mfma_scale_f32_16x16x128_f8f6f4 v[42:45], v[10:17], v[222:229], v[42:45], v232, v232 op_sel_hi:[0,0,0]
	v_mfma_scale_f32_16x16x128_f8f6f4 v[38:41], v[26:33], v[222:229], v[38:41], v232, v232 op_sel_hi:[0,0,0]
	v_mfma_scale_f32_16x16x128_f8f6f4 v[94:97], v[2:9], v[194:201], v[94:97], v232, v232 op_sel_hi:[0,0,0]
	v_mfma_scale_f32_16x16x128_f8f6f4 v[86:89], v[18:25], v[194:201], v[86:89], v232, v232 op_sel_hi:[0,0,0]
	v_mfma_scale_f32_16x16x128_f8f6f4 v[78:81], v[2:9], v[202:209], v[78:81], v232, v232 op_sel_hi:[0,0,0]
	v_mfma_scale_f32_16x16x128_f8f6f4 v[70:73], v[18:25], v[202:209], v[70:73], v232, v232 op_sel_hi:[0,0,0]
	v_mfma_scale_f32_16x16x128_f8f6f4 v[62:65], v[2:9], v[210:217], v[62:65], v232, v232 op_sel_hi:[0,0,0]
	v_mfma_scale_f32_16x16x128_f8f6f4 v[54:57], v[18:25], v[210:217], v[54:57], v232, v232 op_sel_hi:[0,0,0]
	v_mfma_scale_f32_16x16x128_f8f6f4 v[46:49], v[2:9], v[222:229], v[46:49], v232, v232 op_sel_hi:[0,0,0]
	v_mfma_scale_f32_16x16x128_f8f6f4 v[34:37], v[18:25], v[222:229], v[34:37], v232, v232 op_sel_hi:[0,0,0]
	s_setprio 0
	s_barrier
	ds_read_b128 v[2:5], v192
	ds_read_b128 v[6:9], v192 offset:1024
	ds_read_b128 v[10:13], v192 offset:2048
	ds_read_b128 v[14:17], v192 offset:3072
	ds_read_b128 v[18:21], v193
	ds_read_b128 v[22:25], v193 offset:1024
	ds_read_b128 v[26:29], v193 offset:2048
	ds_read_b128 v[30:33], v193 offset:3072
	s_mov_b32 m0, s48
	v_lshl_add_u64 v[216:217], s[6:7], 0, v[218:219]
	ds_read_b128 v[192:195], v191 offset:32768
	ds_read_b128 v[196:199], v191 offset:33792
	ds_read_b128 v[200:203], v191 offset:34816
	ds_read_b128 v[204:207], v191 offset:35840
	ds_read_b128 v[208:211], v191 offset:36864
	ds_read_b128 v[212:215], v191 offset:37888
	ds_read_b128 v[222:225], v191 offset:38912
	ds_read_b128 v[226:229], v191 offset:39936
	global_load_lds_dwordx4 v[216:217], off
	s_mov_b32 m0, s49
	v_lshl_add_u64 v[216:217], s[6:7], 0, v[172:173]
	global_load_lds_dwordx4 v[216:217], off
	s_waitcnt vmcnt(8)
	s_waitcnt lgkmcnt(0)
	s_barrier
	s_setprio 1
	v_mfma_scale_f32_16x16x128_f8f6f4 v[154:157], v[2:9], v[192:199], v[154:157], v232, v232 op_sel_hi:[0,0,0]
	v_mfma_scale_f32_16x16x128_f8f6f4 v[146:149], v[10:17], v[192:199], v[146:149], v232, v232 op_sel_hi:[0,0,0]
	v_mfma_scale_f32_16x16x128_f8f6f4 v[138:141], v[2:9], v[200:207], v[138:141], v232, v232 op_sel_hi:[0,0,0]
	v_mfma_scale_f32_16x16x128_f8f6f4 v[130:133], v[10:17], v[200:207], v[130:133], v232, v232 op_sel_hi:[0,0,0]
	v_mfma_scale_f32_16x16x128_f8f6f4 v[122:125], v[2:9], v[208:215], v[122:125], v232, v232 op_sel_hi:[0,0,0]
	v_mfma_scale_f32_16x16x128_f8f6f4 v[114:117], v[10:17], v[208:215], v[114:117], v232, v232 op_sel_hi:[0,0,0]
	v_mfma_scale_f32_16x16x128_f8f6f4 v[106:109], v[2:9], v[222:229], v[106:109], v232, v232 op_sel_hi:[0,0,0]
	v_mfma_scale_f32_16x16x128_f8f6f4 v[98:101], v[10:17], v[222:229], v[98:101], v232, v232 op_sel_hi:[0,0,0]
	v_mfma_scale_f32_16x16x128_f8f6f4 v[158:161], v[18:25], v[192:199], v[158:161], v232, v232 op_sel_hi:[0,0,0]
	v_mfma_scale_f32_16x16x128_f8f6f4 v[150:153], v[26:33], v[192:199], v[150:153], v232, v232 op_sel_hi:[0,0,0]
	v_mfma_scale_f32_16x16x128_f8f6f4 v[142:145], v[18:25], v[200:207], v[142:145], v232, v232 op_sel_hi:[0,0,0]
	v_mfma_scale_f32_16x16x128_f8f6f4 v[134:137], v[26:33], v[200:207], v[134:137], v232, v232 op_sel_hi:[0,0,0]
	v_mfma_scale_f32_16x16x128_f8f6f4 v[126:129], v[18:25], v[208:215], v[126:129], v232, v232 op_sel_hi:[0,0,0]
	v_mfma_scale_f32_16x16x128_f8f6f4 v[118:121], v[26:33], v[208:215], v[118:121], v232, v232 op_sel_hi:[0,0,0]
	v_mfma_scale_f32_16x16x128_f8f6f4 v[110:113], v[18:25], v[222:229], v[110:113], v232, v232 op_sel_hi:[0,0,0]
	v_mfma_scale_f32_16x16x128_f8f6f4 v[102:105], v[26:33], v[222:229], v[102:105], v232, v232 op_sel_hi:[0,0,0]
	s_setprio 0
	s_barrier
	s_mov_b32 m0, s51
	v_lshl_add_u64 v[178:179], v[178:179], 0, s[72:73]
	ds_read_b128 v[192:195], v191 offset:49152
	ds_read_b128 v[196:199], v191 offset:50176
	ds_read_b128 v[200:203], v191 offset:51200
	ds_read_b128 v[204:207], v191 offset:52224
	ds_read_b128 v[208:211], v191 offset:53248
	ds_read_b128 v[212:215], v191 offset:54272
	ds_read_b128 v[222:225], v191 offset:55296
	ds_read_b128 v[226:229], v191 offset:56320
	global_load_lds_dwordx4 v[178:179], off
	s_mov_b32 m0, s56
	v_lshl_add_u64 v[178:179], v[180:181], 0, s[72:73]
	global_load_lds_dwordx4 v[178:179], off
	s_mov_b32 m0, s62
	v_lshl_add_u64 v[178:179], v[182:183], 0, s[72:73]
	global_load_lds_dwordx4 v[178:179], off
	s_mov_b32 m0, s63
	v_lshl_add_u64 v[178:179], v[184:185], 0, s[72:73]
	global_load_lds_dwordx4 v[178:179], off
	s_mov_b32 m0, s57
	v_lshl_add_u64 v[178:179], v[186:187], 0, s[72:73]
	global_load_lds_dwordx4 v[178:179], off
	s_mov_b32 m0, s60
	v_lshl_add_u64 v[178:179], v[188:189], 0, s[72:73]
	global_load_lds_dwordx4 v[178:179], off
	s_waitcnt vmcnt(8)
	s_waitcnt lgkmcnt(0)
	s_barrier
	s_setprio 1
	v_mfma_scale_f32_16x16x128_f8f6f4 v[90:93], v[2:9], v[192:199], v[90:93], v232, v232 op_sel_hi:[0,0,0]
	v_mfma_scale_f32_16x16x128_f8f6f4 v[82:85], v[10:17], v[192:199], v[82:85], v232, v232 op_sel_hi:[0,0,0]
	v_mfma_scale_f32_16x16x128_f8f6f4 v[74:77], v[2:9], v[200:207], v[74:77], v232, v232 op_sel_hi:[0,0,0]
	v_mfma_scale_f32_16x16x128_f8f6f4 v[66:69], v[10:17], v[200:207], v[66:69], v232, v232 op_sel_hi:[0,0,0]
	v_mfma_scale_f32_16x16x128_f8f6f4 v[58:61], v[2:9], v[208:215], v[58:61], v232, v232 op_sel_hi:[0,0,0]
	v_mfma_scale_f32_16x16x128_f8f6f4 v[50:53], v[10:17], v[208:215], v[50:53], v232, v232 op_sel_hi:[0,0,0]
	v_mfma_scale_f32_16x16x128_f8f6f4 v[42:45], v[2:9], v[222:229], v[42:45], v232, v232 op_sel_hi:[0,0,0]
	v_mfma_scale_f32_16x16x128_f8f6f4 v[38:41], v[10:17], v[222:229], v[38:41], v232, v232 op_sel_hi:[0,0,0]
	v_mfma_scale_f32_16x16x128_f8f6f4 v[94:97], v[18:25], v[192:199], v[94:97], v232, v232 op_sel_hi:[0,0,0]
	v_mfma_scale_f32_16x16x128_f8f6f4 v[86:89], v[26:33], v[192:199], v[86:89], v232, v232 op_sel_hi:[0,0,0]
	v_mfma_scale_f32_16x16x128_f8f6f4 v[78:81], v[18:25], v[200:207], v[78:81], v232, v232 op_sel_hi:[0,0,0]
	v_mfma_scale_f32_16x16x128_f8f6f4 v[70:73], v[26:33], v[200:207], v[70:73], v232, v232 op_sel_hi:[0,0,0]
	v_mfma_scale_f32_16x16x128_f8f6f4 v[62:65], v[18:25], v[208:215], v[62:65], v232, v232 op_sel_hi:[0,0,0]
	v_mfma_scale_f32_16x16x128_f8f6f4 v[54:57], v[26:33], v[208:215], v[54:57], v232, v232 op_sel_hi:[0,0,0]
	v_mfma_scale_f32_16x16x128_f8f6f4 v[46:49], v[18:25], v[222:229], v[46:49], v232, v232 op_sel_hi:[0,0,0]
	v_mfma_scale_f32_16x16x128_f8f6f4 v[34:37], v[26:33], v[222:229], v[34:37], v232, v232 op_sel_hi:[0,0,0]
	s_setprio 0
	s_barrier
	s_andn2_b64 vcc, exec, s[16:17]
	s_cbranch_vccnz .LBB0_1284
	s_barrier

.LBB0_1351:
	s_mov_b32 m0, s47
	ds_read_b128 v[198:201], v197 offset:16384
	ds_read_b128 v[202:205], v197 offset:17408
	ds_read_b128 v[206:209], v197 offset:18432
	ds_read_b128 v[210:213], v197 offset:19456
	ds_read_b128 v[42:45], v197 offset:20480
	ds_read_b128 v[46:49], v197 offset:21504
	ds_read_b128 v[34:37], v197 offset:22528
	ds_read_b128 v[38:41], v197 offset:23552
	global_load_lds_dwordx4 v178, s[88:89]
	s_mov_b32 m0, s48
	v_lshl_add_u64 v[192:193], s[80:81], 0, v[218:219]
	global_load_lds_dwordx4 v182, s[88:89]
	s_mov_b32 m0, s50
	v_lshl_add_u64 v[194:195], s[80:81], 0, v[180:181]
	global_load_lds_dwordx4 v178, s[34:35]
	s_mov_b32 m0, s51
	v_mov_b32_e32 v179, v219
	global_load_lds_dwordx4 v182, s[34:35]
	s_mov_b32 m0, s94
	v_mov_b32_e32 v183, v219
	global_load_lds_dwordx4 v[192:193], off
	s_mov_b32 m0, s95
	v_lshl_add_u64 v[184:185], s[88:89], 0, v[178:179]
	global_load_lds_dwordx4 v[194:195], off
	s_waitcnt vmcnt(8)
	s_waitcnt lgkmcnt(0)
	v_lshl_add_u64 v[186:187], s[88:89], 0, v[182:183]
	v_lshl_add_u64 v[188:189], s[34:35], 0, v[178:179]
	v_lshl_add_u64 v[190:191], s[34:35], 0, v[182:183]
	s_barrier
	s_setprio 1
	s_waitcnt lgkmcnt(0)
	v_mfma_scale_f32_16x16x128_f8f6f4 v[110:113], v[18:25], v[198:205], v[110:113], v232, v232 op_sel_hi:[0,0,0]
	v_mfma_scale_f32_16x16x128_f8f6f4 v[106:109], v[26:33], v[198:205], v[106:109], v232, v232 op_sel_hi:[0,0,0]
	v_mfma_scale_f32_16x16x128_f8f6f4 v[94:97], v[18:25], v[206:213], v[94:97], v232, v232 op_sel_hi:[0,0,0]
	v_mfma_scale_f32_16x16x128_f8f6f4 v[90:93], v[26:33], v[206:213], v[90:93], v232, v232 op_sel_hi:[0,0,0]
	v_mfma_scale_f32_16x16x128_f8f6f4 v[78:81], v[18:25], v[42:49], v[78:81], v232, v232 op_sel_hi:[0,0,0]
	v_mfma_scale_f32_16x16x128_f8f6f4 v[74:77], v[26:33], v[42:49], v[74:77], v232, v232 op_sel_hi:[0,0,0]
	v_mfma_scale_f32_16x16x128_f8f6f4 v[62:65], v[18:25], v[34:41], v[62:65], v232, v232 op_sel_hi:[0,0,0]
	v_mfma_scale_f32_16x16x128_f8f6f4 v[58:61], v[26:33], v[34:41], v[58:61], v232, v232 op_sel_hi:[0,0,0]
	v_mfma_scale_f32_16x16x128_f8f6f4 v[102:105], v[2:9], v[198:205], v[102:105], v232, v232 op_sel_hi:[0,0,0]
	v_mfma_scale_f32_16x16x128_f8f6f4 v[98:101], v[10:17], v[198:205], v[98:101], v232, v232 op_sel_hi:[0,0,0]
	v_mfma_scale_f32_16x16x128_f8f6f4 v[86:89], v[2:9], v[206:213], v[86:89], v232, v232 op_sel_hi:[0,0,0]
	v_mfma_scale_f32_16x16x128_f8f6f4 v[82:85], v[10:17], v[206:213], v[82:85], v232, v232 op_sel_hi:[0,0,0]
	v_mfma_scale_f32_16x16x128_f8f6f4 v[70:73], v[2:9], v[42:49], v[70:73], v232, v232 op_sel_hi:[0,0,0]
	v_mfma_scale_f32_16x16x128_f8f6f4 v[66:69], v[10:17], v[42:49], v[66:69], v232, v232 op_sel_hi:[0,0,0]
	v_mfma_scale_f32_16x16x128_f8f6f4 v[54:57], v[2:9], v[34:41], v[54:57], v232, v232 op_sel_hi:[0,0,0]
	v_mfma_scale_f32_16x16x128_f8f6f4 v[50:53], v[10:17], v[34:41], v[50:53], v232, v232 op_sel_hi:[0,0,0]
	s_setprio 0
	s_barrier
	v_add_u32_e32 v14, s83, v196
	v_add_u32_e32 v30, s55, v196
	ds_read_b128 v[2:5], v14
	ds_read_b128 v[6:9], v14 offset:1024
	ds_read_b128 v[10:13], v14 offset:2048
	ds_read_b128 v[14:17], v14 offset:3072
	ds_read_b128 v[18:21], v30
	ds_read_b128 v[22:25], v30 offset:1024
	ds_read_b128 v[26:29], v30 offset:2048
	ds_read_b128 v[30:33], v30 offset:3072
	s_mov_b32 m0, s38
	v_lshl_add_u64 v[214:215], s[62:63], 0, v[218:219]
	ds_read_b128 v[34:37], v197 offset:32768
	ds_read_b128 v[38:41], v197 offset:33792
	ds_read_b128 v[42:45], v197 offset:34816
	ds_read_b128 v[46:49], v197 offset:35840
	ds_read_b128 v[198:201], v197 offset:36864
	ds_read_b128 v[202:205], v197 offset:37888
	ds_read_b128 v[206:209], v197 offset:38912
	ds_read_b128 v[210:213], v197 offset:39936
	global_load_lds_dwordx4 v[214:215], off
	s_mov_b32 m0, s66
	v_lshl_add_u64 v[214:215], s[62:63], 0, v[180:181]
	global_load_lds_dwordx4 v[214:215], off
	s_waitcnt vmcnt(8)
	s_waitcnt lgkmcnt(0)
	s_barrier
	s_setprio 1
	v_mfma_scale_f32_16x16x128_f8f6f4 v[174:177], v[2:9], v[34:41], v[174:177], v232, v232 op_sel_hi:[0,0,0]
	v_mfma_scale_f32_16x16x128_f8f6f4 v[170:173], v[10:17], v[34:41], v[170:173], v232, v232 op_sel_hi:[0,0,0]
	v_mfma_scale_f32_16x16x128_f8f6f4 v[158:161], v[2:9], v[42:49], v[158:161], v232, v232 op_sel_hi:[0,0,0]
	v_mfma_scale_f32_16x16x128_f8f6f4 v[154:157], v[10:17], v[42:49], v[154:157], v232, v232 op_sel_hi:[0,0,0]
	v_mfma_scale_f32_16x16x128_f8f6f4 v[142:145], v[2:9], v[198:205], v[142:145], v232, v232 op_sel_hi:[0,0,0]
	v_mfma_scale_f32_16x16x128_f8f6f4 v[138:141], v[10:17], v[198:205], v[138:141], v232, v232 op_sel_hi:[0,0,0]
	v_mfma_scale_f32_16x16x128_f8f6f4 v[126:129], v[2:9], v[206:213], v[126:129], v232, v232 op_sel_hi:[0,0,0]
	v_mfma_scale_f32_16x16x128_f8f6f4 v[122:125], v[10:17], v[206:213], v[122:125], v232, v232 op_sel_hi:[0,0,0]
	v_mfma_scale_f32_16x16x128_f8f6f4 v[166:169], v[18:25], v[34:41], v[166:169], v232, v232 op_sel_hi:[0,0,0]
	v_mfma_scale_f32_16x16x128_f8f6f4 v[162:165], v[26:33], v[34:41], v[162:165], v232, v232 op_sel_hi:[0,0,0]
	v_mfma_scale_f32_16x16x128_f8f6f4 v[150:153], v[18:25], v[42:49], v[150:153], v232, v232 op_sel_hi:[0,0,0]
	v_mfma_scale_f32_16x16x128_f8f6f4 v[146:149], v[26:33], v[42:49], v[146:149], v232, v232 op_sel_hi:[0,0,0]
	v_mfma_scale_f32_16x16x128_f8f6f4 v[134:137], v[18:25], v[198:205], v[134:137], v232, v232 op_sel_hi:[0,0,0]
	v_mfma_scale_f32_16x16x128_f8f6f4 v[130:133], v[26:33], v[198:205], v[130:133], v232, v232 op_sel_hi:[0,0,0]
	v_mfma_scale_f32_16x16x128_f8f6f4 v[118:121], v[18:25], v[206:213], v[118:121], v232, v232 op_sel_hi:[0,0,0]
	v_mfma_scale_f32_16x16x128_f8f6f4 v[114:117], v[26:33], v[206:213], v[114:117], v232, v232 op_sel_hi:[0,0,0]
	s_setprio 0
	s_barrier
	s_mov_b32 m0, s52
	v_lshl_add_u64 v[184:185], v[184:185], 0, s[72:73]
	ds_read_b128 v[34:37], v197 offset:49152
	ds_read_b128 v[38:41], v197 offset:50176
	ds_read_b128 v[42:45], v197 offset:51200
	ds_read_b128 v[46:49], v197 offset:52224
	ds_read_b128 v[198:201], v197 offset:53248
	ds_read_b128 v[202:205], v197 offset:54272
	ds_read_b128 v[206:209], v197 offset:55296
	ds_read_b128 v[210:213], v197 offset:56320
	global_load_lds_dwordx4 v[184:185], off
	s_mov_b32 m0, s82
	v_lshl_add_u64 v[184:185], v[186:187], 0, s[72:73]
	global_load_lds_dwordx4 v[184:185], off
	s_mov_b32 m0, s96
	v_lshl_add_u64 v[184:185], v[188:189], 0, s[72:73]
	global_load_lds_dwordx4 v[184:185], off
	s_mov_b32 m0, s97
	v_lshl_add_u64 v[184:185], v[190:191], 0, s[72:73]
	global_load_lds_dwordx4 v[184:185], off
	s_mov_b32 m0, s53
	v_lshl_add_u64 v[184:185], v[192:193], 0, s[72:73]
	global_load_lds_dwordx4 v[184:185], off
	s_mov_b32 m0, s54
	v_lshl_add_u64 v[184:185], v[194:195], 0, s[72:73]
	global_load_lds_dwordx4 v[184:185], off
	s_waitcnt vmcnt(8)
	s_waitcnt lgkmcnt(0)
	s_barrier
	s_setprio 1
	v_mfma_scale_f32_16x16x128_f8f6f4 v[110:113], v[2:9], v[34:41], v[110:113], v232, v232 op_sel_hi:[0,0,0]
	v_mfma_scale_f32_16x16x128_f8f6f4 v[106:109], v[10:17], v[34:41], v[106:109], v232, v232 op_sel_hi:[0,0,0]
	v_mfma_scale_f32_16x16x128_f8f6f4 v[94:97], v[2:9], v[42:49], v[94:97], v232, v232 op_sel_hi:[0,0,0]
	v_mfma_scale_f32_16x16x128_f8f6f4 v[90:93], v[10:17], v[42:49], v[90:93], v232, v232 op_sel_hi:[0,0,0]
	v_mfma_scale_f32_16x16x128_f8f6f4 v[78:81], v[2:9], v[198:205], v[78:81], v232, v232 op_sel_hi:[0,0,0]
	v_mfma_scale_f32_16x16x128_f8f6f4 v[74:77], v[10:17], v[198:205], v[74:77], v232, v232 op_sel_hi:[0,0,0]
	v_mfma_scale_f32_16x16x128_f8f6f4 v[62:65], v[2:9], v[206:213], v[62:65], v232, v232 op_sel_hi:[0,0,0]
	v_mfma_scale_f32_16x16x128_f8f6f4 v[58:61], v[10:17], v[206:213], v[58:61], v232, v232 op_sel_hi:[0,0,0]
	v_mfma_scale_f32_16x16x128_f8f6f4 v[102:105], v[18:25], v[34:41], v[102:105], v232, v232 op_sel_hi:[0,0,0]
	v_mfma_scale_f32_16x16x128_f8f6f4 v[98:101], v[26:33], v[34:41], v[98:101], v232, v232 op_sel_hi:[0,0,0]
	v_mfma_scale_f32_16x16x128_f8f6f4 v[86:89], v[18:25], v[42:49], v[86:89], v232, v232 op_sel_hi:[0,0,0]
	v_mfma_scale_f32_16x16x128_f8f6f4 v[82:85], v[26:33], v[42:49], v[82:85], v232, v232 op_sel_hi:[0,0,0]
	v_mfma_scale_f32_16x16x128_f8f6f4 v[70:73], v[18:25], v[198:205], v[70:73], v232, v232 op_sel_hi:[0,0,0]
	v_mfma_scale_f32_16x16x128_f8f6f4 v[66:69], v[26:33], v[198:205], v[66:69], v232, v232 op_sel_hi:[0,0,0]
	v_mfma_scale_f32_16x16x128_f8f6f4 v[54:57], v[18:25], v[206:213], v[54:57], v232, v232 op_sel_hi:[0,0,0]
	v_mfma_scale_f32_16x16x128_f8f6f4 v[50:53], v[26:33], v[206:213], v[50:53], v232, v232 op_sel_hi:[0,0,0]
	s_setprio 0
	s_barrier
	s_add_i32 s93, s93, 2
	s_add_u32 s60, s60, 0x100
	s_addc_u32 s61, s61, 0
	s_cmp_gt_u32 s93, 5
	s_cbranch_scc1 .LBB0_1361
.LBB0_1352:
	s_waitcnt vmcnt(0)
	v_add_u32_e32 v2, s7, v196
	v_add_u32_e32 v14, s49, v196
	ds_read_b128 v[18:21], v2
	ds_read_b128 v[22:25], v2 offset:1024
	ds_read_b128 v[26:29], v2 offset:2048
	ds_read_b128 v[30:33], v2 offset:3072
	ds_read_b128 v[2:5], v14
	ds_read_b128 v[6:9], v14 offset:1024
	ds_read_b128 v[10:13], v14 offset:2048
	ds_read_b128 v[14:17], v14 offset:3072
	s_add_u32 s34, s26, s60
	s_addc_u32 s35, s27, s61
	v_lshl_add_u64 v[192:193], s[34:35], 0, v[218:219]
	v_lshl_add_u64 v[192:193], v[192:193], 0, s[74:75]
	s_add_i32 m0, s94, 0xc000
	v_mov_b32_e32 v181, v219
	ds_read_b128 v[34:37], v197
	ds_read_b128 v[38:41], v197 offset:1024
	ds_read_b128 v[42:45], v197 offset:2048
	ds_read_b128 v[46:49], v197 offset:3072
	ds_read_b128 v[184:187], v197 offset:4096
	ds_read_b128 v[188:191], v197 offset:5120
	ds_read_b128 v[198:201], v197 offset:6144
	ds_read_b128 v[202:205], v197 offset:7168
	global_load_lds_dwordx4 v[192:193], off
	v_lshl_add_u64 v[192:193], s[34:35], 0, v[180:181]
	v_lshl_add_u64 v[192:193], v[192:193], 0, s[74:75]
	s_add_i32 m0, s94, 0xe000
	s_nop 0
	global_load_lds_dwordx4 v[192:193], off
	s_waitcnt vmcnt(8)
	s_waitcnt lgkmcnt(0)
	s_barrier
	s_setprio 1
	v_mfma_scale_f32_16x16x128_f8f6f4 v[174:177], v[18:25], v[34:41], v[174:177], v232, v232 op_sel_hi:[0,0,0]
	v_mfma_scale_f32_16x16x128_f8f6f4 v[170:173], v[26:33], v[34:41], v[170:173], v232, v232 op_sel_hi:[0,0,0]
	v_mfma_scale_f32_16x16x128_f8f6f4 v[158:161], v[18:25], v[42:49], v[158:161], v232, v232 op_sel_hi:[0,0,0]
	v_mfma_scale_f32_16x16x128_f8f6f4 v[154:157], v[26:33], v[42:49], v[154:157], v232, v232 op_sel_hi:[0,0,0]
	v_mfma_scale_f32_16x16x128_f8f6f4 v[142:145], v[18:25], v[184:191], v[142:145], v232, v232 op_sel_hi:[0,0,0]
	v_mfma_scale_f32_16x16x128_f8f6f4 v[138:141], v[26:33], v[184:191], v[138:141], v232, v232 op_sel_hi:[0,0,0]
	v_mfma_scale_f32_16x16x128_f8f6f4 v[126:129], v[18:25], v[198:205], v[126:129], v232, v232 op_sel_hi:[0,0,0]
	v_mfma_scale_f32_16x16x128_f8f6f4 v[122:125], v[26:33], v[198:205], v[122:125], v232, v232 op_sel_hi:[0,0,0]
	v_mfma_scale_f32_16x16x128_f8f6f4 v[166:169], v[2:9], v[34:41], v[166:169], v232, v232 op_sel_hi:[0,0,0]
	v_mfma_scale_f32_16x16x128_f8f6f4 v[162:165], v[10:17], v[34:41], v[162:165], v232, v232 op_sel_hi:[0,0,0]
	v_mfma_scale_f32_16x16x128_f8f6f4 v[150:153], v[2:9], v[42:49], v[150:153], v232, v232 op_sel_hi:[0,0,0]
	v_mfma_scale_f32_16x16x128_f8f6f4 v[146:149], v[10:17], v[42:49], v[146:149], v232, v232 op_sel_hi:[0,0,0]
	v_mfma_scale_f32_16x16x128_f8f6f4 v[134:137], v[2:9], v[184:191], v[134:137], v232, v232 op_sel_hi:[0,0,0]
	v_mfma_scale_f32_16x16x128_f8f6f4 v[130:133], v[10:17], v[184:191], v[130:133], v232, v232 op_sel_hi:[0,0,0]
	v_mfma_scale_f32_16x16x128_f8f6f4 v[118:121], v[2:9], v[198:205], v[118:121], v232, v232 op_sel_hi:[0,0,0]
	v_mfma_scale_f32_16x16x128_f8f6f4 v[114:117], v[10:17], v[198:205], v[114:117], v232, v232 op_sel_hi:[0,0,0]
	s_cmpk_lg_i32 s60, 0x300
	s_setprio 0
	s_barrier
	s_mov_b64 s[90:91], -1
	s_cbranch_scc0 .LBB0_1354
	s_add_u32 s3, s26, s60
	s_addc_u32 s34, s27, s61
	s_add_u32 s80, s3, 0x100
	s_addc_u32 s81, s34, 0
	s_add_u32 s35, s24, s60
	s_addc_u32 s58, s25, s61
	s_add_u32 s88, s35, 0x100
	s_addc_u32 s89, s58, 0
	s_add_u32 s62, s3, 0x20100
	s_addc_u32 s63, s34, 0
	s_add_u32 s34, s35, 0x20100
	s_addc_u32 s35, s58, 0
	s_mov_b64 s[90:91], 0
